# MoE GEMMs: short last row tile of an expert (<=128 valid rows) skips the MFMAs of its padded upper half
# baseline (speedup 1.0000x reference)
; #define SBAR() __builtin_amdgcn_sched_barrier(0)
; #define ATT_SYNC(jn) do { ATT_WAIT_BAR(); if ((jn) < NT) ATT_DMA((jn), (jn) & 3); } while (0)
; __device__ __forceinline__ void attn_dma_body(const bf16_t* __restrict__ Qb, int ldq, int tpos0, const float* __restrict__ rope, const float* __restrict__ qgain, ...
;     ...
;   for (int j = 1; j + 1 < NT; j += 2) {
;     { SBAR(); qkt(pB0, pB1, (const bf16_t*)(lds + (j & 3) * SHM_SLOT), qr, r32, hi);
;       finishSM(pA0, pA1, alA, l_reg, pa0, pa1, pa2, pa3); s16x4 va[8]; pv_rd<0>(va, vb0 + ((j - 1) & 3) * (int)SHM_SLOT); SBAR();
;       if (!lead) ATT_SYNC(j + 2);
;       pv_d0_pre(o, vb0 + ((j - 1) & 3) * (int)SHM_SLOT, va, pa0, pa1, pa2, pa3); partialSM(pB0, pB1, m_reg, mnB, alB);
;       if (lead) ATT_SYNC(j + 2);
.Lf16_loop:
	s_lshl_b32 s36, s97, 15
	s_and_b32 s36, s36, 0x18000
	s_add_i32 s37, s36, 0x18000
	s_and_b32 s37, s37, 0x18000
	v_add_u32_e32 v187, s36, v183
	v_add_u32_e32 v188, s36, v184
	v_add_u32_e32 v189, s36, v185
	v_add_u32_e32 v190, s36, v186
	ds_read_b128 v[146:149], v187 offset:0
	ds_read_b128 v[150:153], v187 offset:4096
	ds_read_b128 v[154:157], v187 offset:8192
	ds_read_b128 v[158:161], v187 offset:12288
	ds_read_b128 v[198:201], v188 offset:0
	ds_read_b128 v[202:205], v188 offset:4096
	ds_read_b128 v[206:209], v188 offset:8192
	ds_read_b128 v[210:213], v188 offset:12288
	v_add_u32_e32 v193, s37, v191
	v_add_u32_e32 v194, s37, v192
	s_waitcnt lgkmcnt(7)
	v_mfma_f32_16x16x32_bf16 v[66:69], v[146:149], v[98:101], 0
	v_mfma_f32_16x16x32_bf16 v[70:73], v[146:149], v[114:117], 0
	ds_read_b128 v[146:149], v189 offset:0
	s_waitcnt lgkmcnt(7)
	v_mfma_f32_16x16x32_bf16 v[74:77], v[150:153], v[98:101], 0
	v_mfma_f32_16x16x32_bf16 v[78:81], v[150:153], v[114:117], 0
	ds_read_b128 v[150:153], v189 offset:4096
	s_waitcnt lgkmcnt(7)
	v_mfma_f32_16x16x32_bf16 v[82:85], v[154:157], v[98:101], 0
	v_mfma_f32_16x16x32_bf16 v[86:89], v[154:157], v[114:117], 0
	ds_read_b128 v[154:157], v189 offset:8192
	s_waitcnt lgkmcnt(7)
	v_mfma_f32_16x16x32_bf16 v[90:93], v[158:161], v[98:101], 0
	v_mfma_f32_16x16x32_bf16 v[94:97], v[158:161], v[114:117], 0
	ds_read_b128 v[158:161], v189 offset:12288
	s_waitcnt lgkmcnt(7)
	v_mfma_f32_16x16x32_bf16 v[66:69], v[198:201], v[102:105], v[66:69]
	v_mfma_f32_16x16x32_bf16 v[70:73], v[198:201], v[118:121], v[70:73]
	ds_read_b128 v[198:201], v190 offset:0
	s_waitcnt lgkmcnt(7)
	v_mfma_f32_16x16x32_bf16 v[74:77], v[202:205], v[102:105], v[74:77]
	v_mfma_f32_16x16x32_bf16 v[78:81], v[202:205], v[118:121], v[78:81]
	ds_read_b128 v[202:205], v190 offset:4096
	s_waitcnt lgkmcnt(7)
	v_mfma_f32_16x16x32_bf16 v[82:85], v[206:209], v[102:105], v[82:85]
	v_mfma_f32_16x16x32_bf16 v[86:89], v[206:209], v[118:121], v[86:89]
	ds_read_b128 v[206:209], v190 offset:8192
	s_waitcnt lgkmcnt(7)
	v_mfma_f32_16x16x32_bf16 v[90:93], v[210:213], v[102:105], v[90:93]
	v_mfma_f32_16x16x32_bf16 v[94:97], v[210:213], v[118:121], v[94:97]
	ds_read_b128 v[210:213], v190 offset:12288
	s_waitcnt lgkmcnt(7)
	v_mfma_f32_16x16x32_bf16 v[66:69], v[146:149], v[106:109], v[66:69]
	v_mfma_f32_16x16x32_bf16 v[70:73], v[146:149], v[122:125], v[70:73]
	s_waitcnt lgkmcnt(6)
	v_mfma_f32_16x16x32_bf16 v[74:77], v[150:153], v[106:109], v[74:77]
	v_mfma_f32_16x16x32_bf16 v[78:81], v[150:153], v[122:125], v[78:81]
	s_waitcnt lgkmcnt(5)
	v_mfma_f32_16x16x32_bf16 v[82:85], v[154:157], v[106:109], v[82:85]
	v_mfma_f32_16x16x32_bf16 v[86:89], v[154:157], v[122:125], v[86:89]
	s_waitcnt lgkmcnt(4)
	v_mfma_f32_16x16x32_bf16 v[90:93], v[158:161], v[106:109], v[90:93]
	v_mfma_f32_16x16x32_bf16 v[94:97], v[158:161], v[122:125], v[94:97]
	s_waitcnt lgkmcnt(3)
	v_mfma_f32_16x16x32_bf16 v[66:69], v[198:201], v[110:113], v[66:69]
	v_mfma_f32_16x16x32_bf16 v[70:73], v[198:201], v[126:129], v[70:73]
	ds_read_b64_tr_b16 v[214:215], v193 offset:0
	ds_read_b64_tr_b16 v[216:217], v193 offset:4096
	ds_read_b64_tr_b16 v[218:219], v194 offset:0
	ds_read_b64_tr_b16 v[220:221], v194 offset:4096
	ds_read_b64_tr_b16 v[222:223], v193 offset:512
	ds_read_b64_tr_b16 v[224:225], v193 offset:4608
	ds_read_b64_tr_b16 v[226:227], v194 offset:512
	ds_read_b64_tr_b16 v[228:229], v194 offset:4608
	s_waitcnt lgkmcnt(10)
	v_mfma_f32_16x16x32_bf16 v[74:77], v[202:205], v[110:113], v[74:77]
	v_mfma_f32_16x16x32_bf16 v[78:81], v[202:205], v[126:129], v[78:81]
	s_waitcnt lgkmcnt(9)
	v_mfma_f32_16x16x32_bf16 v[82:85], v[206:209], v[110:113], v[82:85]
	v_mfma_f32_16x16x32_bf16 v[86:89], v[206:209], v[126:129], v[86:89]
	s_waitcnt lgkmcnt(8)
	v_mfma_f32_16x16x32_bf16 v[90:93], v[210:213], v[110:113], v[90:93]
	v_mfma_f32_16x16x32_bf16 v[94:97], v[210:213], v[126:129], v[94:97]
	s_cmp_lt_u32 s42, 4
	s_cbranch_scc1 .Lf16_a
	s_cmp_ge_u32 s97, 131
	s_cbranch_scc1 .Lf16_se_nl
	s_waitcnt vmcnt(0) lgkmcnt(0)
	s_barrier
	s_cmp_ge_u32 s97, 130
	s_cbranch_scc1 .Lf16_se_nl
	s_add_i32 s6, s36, 0x10000
	s_and_b32 s6, s6, 0x18000
	s_add_i32 s6, s6, s96
	s_mov_b32 m0, s6
	s_nop 0
	global_load_lds_dwordx4 v170, s[2:3]
	s_add_i32 m0, s6, 0x2000
	s_nop 0
	global_load_lds_dwordx4 v172, s[2:3]
	s_add_i32 m0, s6, 0x4000
	s_nop 0
	global_load_lds_dwordx4 v171, s[4:5]
	s_add_i32 m0, s6, 0x6000
	s_nop 0
	global_load_lds_dwordx4 v173, s[4:5]
	s_add_u32 s2, s2, 0x4000
	s_addc_u32 s3, s3, 0
	s_add_u32 s4, s4, 0x4000
	s_addc_u32 s5, s5, 0

;     __device__ __forceinline__ bool get(int i, int& pm, int& pn) const { return map((long)i * G + c, pm, pn); }
;     __device__ __forceinline__ bool next(int i, Unit& o) const { if (i != 0) return false; o = u; return true; }
;     __device__ __forceinline__ bool next(int i, Unit& u) const { int pm, pn;
;         if (GATHER) { if (!o.get(i, pm, pn)) return false; }
;         else { const bool light = o.c >= rem; const long L = (light && i < 2) ? (long)i * nl + (o.c - rem) : 2L * nl + (long)(light ? i - 2 : i) * o.G + o.c; if (!o.map(L, pm, pn)) return false; }
;         const int e = __builtin_amdgcn_readfirstlane(texp[pm]);
;         u.pm = pm; u.pn = pn; u.aux = e; u.kt = KT; u.ui = i; u.rb = (pm - __builtin_amdgcn_readfirstlane(tbase[e])) * 256; u.cn = __builtin_amdgcn_readfirstlane(tcnt[e]);
;         u.A = GATHER ? A : A + (size_t)((unsigned)pm * AT); u.B = B + (size_t)((unsigned)e * BE + (unsigned)pn * BT); return true; }
.LBB0_852:
	s_or_b64 exec, exec, s[4:5]
	s_add_u32 s10, s6, 0x4a400000
	s_addc_u32 s11, s7, 0
	s_add_u32 s60, s6, 0x1800000
	v_mov_b32_e32 v10, v0
	v_cndmask_b32_e64 v1, 0, 1, s[12:13]
	s_addc_u32 s61, s7, 0
	s_waitcnt lgkmcnt(0)
	s_barrier
	v_cmp_ne_u32_e64 s[2:3], 1, v1
	s_andn2_b64 vcc, exec, s[12:13]
	v_readfirstlane_b32 s4, v10
	s_cbranch_vccnz .LBB0_854
	s_lshr_b32 s5, s56, 29
	s_add_i32 s5, s51, s5
	s_ashr_i32 s12, s5, 3
	s_and_b32 s5, s5, -8
	s_sub_i32 s5, s51, s5
	s_cmp_lt_i32 s5, 0
	s_cselect_b32 s13, s48, s33
	s_mul_i32 s5, s13, s5
	s_add_i32 s5, s5, s12
	s_ashr_i32 s12, s5, 31
	s_lshr_b32 s12, s12, 26
	s_add_i32 s12, s5, s12
	s_ashr_i32 s13, s12, 6
	s_lshl_b32 s13, s13, 3
	s_sub_i32 s14, s33, s13
	s_min_i32 s14, s14, 8
	s_abs_i32 s15, s14
	v_cvt_f32_u32_e32 v1, s15
	s_sub_i32 s17, 0, s15
	s_andn2_b32 s12, s12, 63
	s_sub_i32 s5, s5, s12
	v_rcp_iflag_f32_e32 v1, v1
	s_abs_i32 s12, s5
	s_xor_b32 s16, s5, s14
	s_ashr_i32 s16, s16, 31
	v_mul_f32_e32 v1, 0x4f7ffffe, v1
	v_cvt_u32_f32_e32 v1, v1
	s_mov_b64 s[34:35], s[10:11]
	v_readfirstlane_b32 s18, v1
	s_mul_i32 s17, s17, s18
	s_mul_hi_u32 s17, s18, s17
	s_add_i32 s18, s18, s17
	s_mul_hi_u32 s17, s12, s18
	s_mul_i32 s18, s17, s15
	s_sub_i32 s12, s12, s18
	s_add_i32 s19, s17, 1
	s_sub_i32 s18, s12, s15
	s_cmp_ge_u32 s12, s15
	s_cselect_b32 s17, s19, s17
	s_cselect_b32 s12, s18, s12
	s_add_i32 s18, s17, 1
	s_cmp_ge_u32 s12, s15
	s_cselect_b32 s12, s18, s17
	s_xor_b32 s12, s12, s16
	s_sub_i32 s77, s12, s16
	s_mul_i32 s12, s77, s14
	s_sub_i32 s5, s5, s12
	s_add_i32 s62, s5, s13
	s_lshl_b32 s5, s62, 2
	s_add_i32 s5, s5, 0
	s_add_i32 s5, s5, 0x20240
	v_mov_b32_e32 v1, s5
	ds_read_b32 v1, v1
	s_lshl_b32 s5, s77, 20
	s_waitcnt lgkmcnt(0)
	v_readfirstlane_b32 s12, v1
	s_lshl_b32 s98, s12, 2
	v_mov_b32_e32 v251, s98
	v_add_u32_e32 v251, 0x20100, v251
	ds_read_b32 v252, v251
	ds_read_b32 v253, v251 offset:128
	s_waitcnt lgkmcnt(0)
	v_readfirstlane_b32 s98, v252
	v_readfirstlane_b32 s100, v253
	s_nop 3
	s_sub_i32 s100, s62, s100
	s_lshl_b32 s100, s100, 8
	s_sub_i32 s98, s98, s100
	s_cmp_le_i32 s98, 128
	s_cselect_b32 s98, 1, 0
	s_lshl_b32 s12, s12, 23
	s_add_i32 s12, s12, s5
	s_add_u32 s40, s60, s12
	s_addc_u32 s41, s61, 0
	s_and_b64 vcc, exec, s[2:3]
	s_cbranch_vccz .LBB0_855
	s_branch .LBB0_905

;     __device__ __forceinline__ bool get(int i, int& pm, int& pn) const { return map((long)i * G + c, pm, pn); }
;     __device__ __forceinline__ bool next(int i, Unit& o) const { if (i != 0) return false; o = u; return true; }
; template <class Epi, class Sched, bool ALIGN_EPI, bool GATHER = false>
; __device__ __forceinline__ void gemm_phase(PG8_LAS unsigned char* lds, const Gemm g, const Sched& S, const Epi& E) {
;     ...
;     for (;;) {
;         const bool has_next = S.next(ui + 1, nxt);
;         if constexpr (Sched::WAITS) wst = has_next ? 1 : 0;
;         const char* nA = has_next ? nxt.A : cA; const char* nB = has_next ? nxt.B : cB;
;     __device__ __forceinline__ bool next(int i, Unit& u) const { int pm, pn;
;         if (GATHER) { if (!o.get(i, pm, pn)) return false; }
;         else { const bool light = o.c >= rem; const long L = (light && i < 2) ? (long)i * nl + (o.c - rem) : 2L * nl + (long)(light ? i - 2 : i) * o.G + o.c; if (!o.map(L, pm, pn)) return false; }
;         const int e = __builtin_amdgcn_readfirstlane(texp[pm]);
;         u.pm = pm; u.pn = pn; u.aux = e; u.kt = KT; u.ui = i; u.rb = (pm - __builtin_amdgcn_readfirstlane(tbase[e])) * 256; u.cn = __builtin_amdgcn_readfirstlane(tcnt[e]);
;         u.A = GATHER ? A : A + (size_t)((unsigned)pm * AT); u.B = B + (size_t)((unsigned)e * BE + (unsigned)pn * BT); return true; }
.LBB0_858:
	s_add_i32 s75, s22, 1
	s_mul_i32 s4, s75, s59
	s_mul_hi_u32 s5, s75, s50
	s_add_i32 s5, s5, s4
	s_mul_i32 s4, s75, s50
	s_add_u32 s42, s4, s51
	s_addc_u32 s43, s5, s56
	v_cmp_ge_i64_e32 vcc, s[42:43], v[140:141]
	s_mov_b32 s74, s62
	s_mov_b32 s99, s98
	v_cmp_lt_i64_e64 s[6:7], s[42:43], v[140:141]
	s_cbranch_vccnz .LBB0_860
	s_ashr_i32 s4, s42, 31
	s_lshr_b32 s4, s4, 29
	s_add_i32 s4, s42, s4
	s_ashr_i32 s5, s4, 3
	s_and_b32 s4, s4, -8
	s_sub_i32 s4, s42, s4
	s_cmp_lt_i32 s4, 0
	s_cselect_b32 s23, s48, s33
	s_mul_i32 s4, s23, s4
	s_add_i32 s4, s4, s5
	s_ashr_i32 s5, s4, 31
	s_lshr_b32 s5, s5, 26
	s_add_i32 s5, s4, s5
	s_ashr_i32 s23, s5, 6
	s_lshl_b32 s23, s23, 3
	s_sub_i32 s36, s33, s23
	s_min_i32 s36, s36, 8
	s_abs_i32 s37, s36
	v_cvt_f32_u32_e32 v2, s37
	s_sub_i32 s39, 0, s37
	s_andn2_b32 s5, s5, 63
	s_sub_i32 s4, s4, s5
	v_rcp_iflag_f32_e32 v2, v2
	s_abs_i32 s5, s4
	s_xor_b32 s38, s4, s36
	s_ashr_i32 s38, s38, 31
	v_mul_f32_e32 v2, 0x4f7ffffe, v2
	v_cvt_u32_f32_e32 v2, v2
	s_nop 0
	v_readfirstlane_b32 s43, v2
	s_mul_i32 s39, s39, s43
	s_mul_hi_u32 s39, s43, s39
	s_add_i32 s43, s43, s39
	s_mul_hi_u32 s39, s5, s43
	s_mul_i32 s43, s39, s37
	s_sub_i32 s5, s5, s43
	s_add_i32 s44, s39, 1
	s_sub_i32 s43, s5, s37
	s_cmp_ge_u32 s5, s37
	s_cselect_b32 s39, s44, s39
	s_cselect_b32 s5, s43, s5
	s_add_i32 s43, s39, 1
	s_cmp_ge_u32 s5, s37
	s_cselect_b32 s5, s43, s39
	s_xor_b32 s5, s5, s38
	s_sub_i32 s76, s5, s38
	s_mul_i32 s5, s76, s36
	s_sub_i32 s4, s4, s5
	s_add_i32 s62, s4, s23
	s_lshl_b32 s4, s62, 2
	s_add_i32 s4, s4, 0
	s_add_i32 s4, s4, 0x20240
	v_mov_b32_e32 v2, s4
	ds_read_b32 v2, v2
	s_lshl_b32 s4, s76, 20
	s_mov_b64 s[38:39], s[10:11]
	s_waitcnt lgkmcnt(0)
	v_readfirstlane_b32 s5, v2
	s_lshl_b32 s98, s5, 2
	v_mov_b32_e32 v251, s98
	v_add_u32_e32 v251, 0x20100, v251
	ds_read_b32 v252, v251
	ds_read_b32 v253, v251 offset:128
	s_waitcnt lgkmcnt(0)
	v_readfirstlane_b32 s98, v252
	v_readfirstlane_b32 s100, v253
	s_nop 3
	s_sub_i32 s100, s62, s100
	s_lshl_b32 s100, s100, 8
	s_sub_i32 s98, s98, s100
	s_cmp_le_i32 s98, 128
	s_cselect_b32 s98, 1, 0
	s_lshl_b32 s5, s5, 23
	s_add_i32 s5, s5, s4
	s_add_u32 s36, s60, s5
	s_addc_u32 s37, s61, 0

; #define PG8_STAGE(bufoff, gbase, voff) do { _Pragma("unroll") for (int _i = 0; _i < 2; ++_i) \
;         __builtin_amdgcn_global_load_lds((const unsigned*)((const char*)(gbase) + (voff)[_i]), (PG8_LAS unsigned*)(lds + (bufoff) + ldsw + _i * 8192), 16, 0, 0); } while (0)
; #define PG8_LDA(dst, b, h) do { _Pragma("unroll") for (int m = 0; m < 4; ++m) _Pragma("unroll") for (int k = 0; k < 2; ++k) dst[m][k] = *(const PG8_LAS bf16x8*)(lds + PG8_SA(b, h) + aoff + m * 2048 + k * 1024); } while (0)
; #define PG8_LDB(dst, b, h) do { _Pragma("unroll") for (int n = 0; n < 2; ++n) _Pragma("unroll") for (int k = 0; k < 2; ++k) dst[n][k] = *(const PG8_LAS bf16x8*)(lds + PG8_SB(b, h) + boff + n * 2048 + k * 1024); } while (0)
; #define PG8_MMA(ai, bj, At, Bt) do { __builtin_amdgcn_s_setprio(1); _Pragma("unroll") for (int m = 0; m < 4; ++m) _Pragma("unroll") for (int n = 0; n < 2; ++n) _Pragma("unroll") for (int k = 0; k < 2; ++k) \
;         acc[ai][bj][m][n] = __builtin_amdgcn_mfma_f32_16x16x32_bf16(Bt[n][k], At[m][k], acc[ai][bj][m][n], 0, 0, 0); __builtin_amdgcn_s_setprio(0); } while (0)
; #define PG8_WAIT_V(n) asm volatile("s_waitcnt vmcnt(" #n ")" ::: "memory")
; #define PG8_WAIT_L(n) asm volatile("s_waitcnt lgkmcnt(" #n ")" ::: "memory")
; #define PG8_BAR __builtin_amdgcn_s_barrier()
; #define PG8_SCHED __builtin_amdgcn_sched_barrier(0)
; template <class Epi, class Sched, bool ALIGN_EPI, bool GATHER = false>
; __device__ __forceinline__ void gemm_phase(PG8_LAS unsigned char* lds, const Gemm g, const Sched& S, const Epi& E) {
;     ...
;             PG8_LDB(B0, 0, 0); PG8_LDB(B1, 0, 1); PG8_SCHED; PG8_LDA(At, 0, 0); PG8_STAGE(PG8_SA(1, 1), a1, vc[1]);
;             PG8_WAIT_V(8); PG8_WAIT_L(0); PG8_BAR; PG8_MMA(0, 0, At, B0); PG8_MMA(0, 1, At, B1); PG8_BAR; PG8_SCHED;
;             PG8_LDA(At, 0, 1); PG8_STAGE(PG8_SB(0, 0), b2, voffB); PG8_STAGE(PG8_SB(0, 1), b2 + hsB, voffB); PG8_STAGE(PG8_SA(0, 0), a2, o0);
;             PG8_WAIT_V(8); PG8_WAIT_L(0); PG8_BAR; PG8_MMA(1, 0, At, B0); PG8_MMA(1, 1, At, B1); PG8_BAR; PG8_SCHED;
.LBB0_889:
	ds_read_b128 v[166:169], v160
	ds_read_b128 v[170:173], v160 offset:1024
	ds_read_b128 v[174:177], v160 offset:2048
	ds_read_b128 v[178:181], v160 offset:3072
	ds_read_b128 v[182:185], v161
	ds_read_b128 v[186:189], v161 offset:1024
	ds_read_b128 v[190:193], v161 offset:2048
	ds_read_b128 v[194:197], v161 offset:3072
	s_add_u32 s40, s34, s6
	s_addc_u32 s41, s35, s7
	s_add_u32 s42, s40, 0x100
	s_addc_u32 s43, s41, 0
	s_add_u32 s45, s22, s6
	s_addc_u32 s46, s23, s7
	s_cmpk_eq_i32 s6, 0xf00
	s_cselect_b64 vcc, -1, 0
	s_and_b64 s[40:41], vcc, exec
	v_cndmask_b32_e32 v138, v142, v164, vcc
	s_cselect_b32 s43, s39, s43
	s_cselect_b32 s42, s38, s42
	v_cndmask_b32_e32 v143, v146, v162, vcc
	v_cndmask_b32_e32 v230, v144, v163, vcc
	v_cndmask_b32_e32 v147, v148, v165, vcc
	s_cselect_b32 s41, s37, s46
	s_cselect_b32 s40, s36, s45
	v_lshl_add_u64 v[232:233], v[152:153], 0, s[6:7]
	s_add_i32 m0, s64, 0xc000
	ds_read_b128 v[198:201], v159
	ds_read_b128 v[202:205], v159 offset:1024
	ds_read_b128 v[206:209], v159 offset:2048
	ds_read_b128 v[210:213], v159 offset:3072
	ds_read_b128 v[214:217], v159 offset:4096
	ds_read_b128 v[218:221], v159 offset:5120
	ds_read_b128 v[222:225], v159 offset:6144
	ds_read_b128 v[226:229], v159 offset:7168
	global_load_lds_dwordx4 v[232:233], off
	v_lshl_add_u64 v[232:233], v[150:151], 0, s[6:7]
	s_add_i32 m0, s64, 0xe000
	s_nop 0
	global_load_lds_dwordx4 v[232:233], off
	s_waitcnt vmcnt(8)
	s_waitcnt lgkmcnt(0)
	s_barrier
	s_setprio 1
	s_waitcnt lgkmcnt(0)
	v_mfma_f32_16x16x32_bf16 v[126:129], v[166:169], v[198:201], v[126:129]
	v_mfma_f32_16x16x32_bf16 v[118:121], v[174:177], v[198:201], v[118:121]
	v_mfma_f32_16x16x32_bf16 v[110:113], v[166:169], v[206:209], v[110:113]
	v_mfma_f32_16x16x32_bf16 v[102:105], v[174:177], v[206:209], v[102:105]
	v_mfma_f32_16x16x32_bf16 v[94:97], v[166:169], v[214:217], v[94:97]
	v_mfma_f32_16x16x32_bf16 v[86:89], v[174:177], v[214:217], v[86:89]
	v_mfma_f32_16x16x32_bf16 v[78:81], v[166:169], v[222:225], v[78:81]
	v_mfma_f32_16x16x32_bf16 v[70:73], v[174:177], v[222:225], v[70:73]
	v_mfma_f32_16x16x32_bf16 v[126:129], v[170:173], v[202:205], v[126:129]
	v_mfma_f32_16x16x32_bf16 v[118:121], v[178:181], v[202:205], v[118:121]
	v_mfma_f32_16x16x32_bf16 v[110:113], v[170:173], v[210:213], v[110:113]
	v_mfma_f32_16x16x32_bf16 v[102:105], v[178:181], v[210:213], v[102:105]
	v_mfma_f32_16x16x32_bf16 v[94:97], v[170:173], v[218:221], v[94:97]
	v_mfma_f32_16x16x32_bf16 v[86:89], v[178:181], v[218:221], v[86:89]
	v_mfma_f32_16x16x32_bf16 v[78:81], v[170:173], v[226:229], v[78:81]
	v_mfma_f32_16x16x32_bf16 v[70:73], v[178:181], v[226:229], v[70:73]
	s_setprio 0
	s_setprio 1
	v_mfma_f32_16x16x32_bf16 v[122:125], v[182:185], v[198:201], v[122:125]
	v_mfma_f32_16x16x32_bf16 v[114:117], v[190:193], v[198:201], v[114:117]
	v_mfma_f32_16x16x32_bf16 v[106:109], v[182:185], v[206:209], v[106:109]
	v_mfma_f32_16x16x32_bf16 v[98:101], v[190:193], v[206:209], v[98:101]
	v_mfma_f32_16x16x32_bf16 v[90:93], v[182:185], v[214:217], v[90:93]
	v_mfma_f32_16x16x32_bf16 v[82:85], v[190:193], v[214:217], v[82:85]
	v_mfma_f32_16x16x32_bf16 v[74:77], v[182:185], v[222:225], v[74:77]
	v_mfma_f32_16x16x32_bf16 v[66:69], v[190:193], v[222:225], v[66:69]
	v_mfma_f32_16x16x32_bf16 v[122:125], v[186:189], v[202:205], v[122:125]
	v_mfma_f32_16x16x32_bf16 v[114:117], v[194:197], v[202:205], v[114:117]
	v_mfma_f32_16x16x32_bf16 v[106:109], v[186:189], v[210:213], v[106:109]
	v_mfma_f32_16x16x32_bf16 v[98:101], v[194:197], v[210:213], v[98:101]
	v_mfma_f32_16x16x32_bf16 v[90:93], v[186:189], v[218:221], v[90:93]
	v_mfma_f32_16x16x32_bf16 v[82:85], v[194:197], v[218:221], v[82:85]
	v_mfma_f32_16x16x32_bf16 v[74:77], v[186:189], v[226:229], v[74:77]
	v_mfma_f32_16x16x32_bf16 v[66:69], v[194:197], v[226:229], v[66:69]
	s_setprio 0
	s_barrier
	s_add_i32 s45, s72, s63
	v_lshl_add_u64 v[232:233], s[40:41], 0, v[132:133]
	s_mov_b32 m0, s45
	ds_read_b128 v[198:201], v159 offset:16384
	ds_read_b128 v[202:205], v159 offset:17408
	ds_read_b128 v[206:209], v159 offset:18432
	ds_read_b128 v[210:213], v159 offset:19456
	ds_read_b128 v[214:217], v159 offset:20480
	ds_read_b128 v[218:221], v159 offset:21504
	ds_read_b128 v[222:225], v159 offset:22528
	ds_read_b128 v[226:229], v159 offset:23552
	global_load_lds_dwordx4 v[232:233], off
	s_add_i32 m0, s45, 0x2000
	s_add_u32 s46, s40, 0x80000
	v_lshl_add_u64 v[234:235], s[40:41], 0, v[136:137]
	s_addc_u32 s47, s41, 0
	s_add_i32 s45, s73, s63
	global_load_lds_dwordx4 v[234:235], off
	v_lshl_add_u64 v[236:237], s[46:47], 0, v[132:133]
	s_mov_b32 m0, s45
	v_mov_b32_e32 v231, v139
	global_load_lds_dwordx4 v[236:237], off
	v_lshl_add_u64 v[236:237], s[46:47], 0, v[136:137]
	s_add_i32 m0, s45, 0x2000
	s_nop 0
	global_load_lds_dwordx4 v[236:237], off
	s_mov_b32 m0, s64
	v_lshl_add_u64 v[236:237], s[42:43], 0, v[138:139]
	global_load_lds_dwordx4 v138, s[42:43]
	s_mov_b32 m0, s65
	s_nop 0
	global_load_lds_dwordx4 v230, s[42:43]
	s_waitcnt vmcnt(8)
	s_waitcnt lgkmcnt(0)
	v_lshl_add_u64 v[230:231], s[42:43], 0, v[230:231]
	s_barrier
	s_setprio 1
	s_cmp_lg_u32 s99, 0
	s_cbranch_scc1 .Lms_1
; #define PG8_STAGE(bufoff, gbase, voff) do { _Pragma("unroll") for (int _i = 0; _i < 2; ++_i) \
;         __builtin_amdgcn_global_load_lds((const unsigned*)((const char*)(gbase) + (voff)[_i]), (PG8_LAS unsigned*)(lds + (bufoff) + ldsw + _i * 8192), 16, 0, 0); } while (0)
; #define PG8_LDA(dst, b, h) do { _Pragma("unroll") for (int m = 0; m < 4; ++m) _Pragma("unroll") for (int k = 0; k < 2; ++k) dst[m][k] = *(const PG8_LAS bf16x8*)(lds + PG8_SA(b, h) + aoff + m * 2048 + k * 1024); } while (0)
; #define PG8_LDB(dst, b, h) do { _Pragma("unroll") for (int n = 0; n < 2; ++n) _Pragma("unroll") for (int k = 0; k < 2; ++k) dst[n][k] = *(const PG8_LAS bf16x8*)(lds + PG8_SB(b, h) + boff + n * 2048 + k * 1024); } while (0)
; #define PG8_MMA(ai, bj, At, Bt) do { __builtin_amdgcn_s_setprio(1); _Pragma("unroll") for (int m = 0; m < 4; ++m) _Pragma("unroll") for (int n = 0; n < 2; ++n) _Pragma("unroll") for (int k = 0; k < 2; ++k) \
;         acc[ai][bj][m][n] = __builtin_amdgcn_mfma_f32_16x16x32_bf16(Bt[n][k], At[m][k], acc[ai][bj][m][n], 0, 0, 0); __builtin_amdgcn_s_setprio(0); } while (0)
; #define PG8_WAIT_V(n) asm volatile("s_waitcnt vmcnt(" #n ")" ::: "memory")
; #define PG8_WAIT_L(n) asm volatile("s_waitcnt lgkmcnt(" #n ")" ::: "memory")
; #define PG8_BAR __builtin_amdgcn_s_barrier()
; #define PG8_SCHED __builtin_amdgcn_sched_barrier(0)
; template <class Epi, class Sched, bool ALIGN_EPI, bool GATHER = false>
; __device__ __forceinline__ void gemm_phase(PG8_LAS unsigned char* lds, const Gemm g, const Sched& S, const Epi& E) {
;     ...
;             PG8_WAIT_V(8); PG8_WAIT_L(0); PG8_BAR; PG8_MMA(1, 0, At, B0); PG8_MMA(1, 1, At, B1); PG8_BAR; PG8_SCHED;
;             PG8_LDB(B0, 1, 0); PG8_LDB(B1, 1, 1); PG8_SCHED; PG8_LDA(At, 1, 0); PG8_STAGE(PG8_SA(0, 1), a2, o1);
;             PG8_WAIT_V(8); PG8_WAIT_L(0); PG8_BAR; PG8_MMA(0, 0, At, B0); PG8_MMA(0, 1, At, B1); PG8_BAR; PG8_SCHED;
	s_waitcnt lgkmcnt(0)
	v_mfma_f32_16x16x32_bf16 v[62:65], v[166:169], v[198:201], v[62:65]
	v_mfma_f32_16x16x32_bf16 v[54:57], v[174:177], v[198:201], v[54:57]
	v_mfma_f32_16x16x32_bf16 v[46:49], v[166:169], v[206:209], v[46:49]
	v_mfma_f32_16x16x32_bf16 v[38:41], v[174:177], v[206:209], v[38:41]
	v_mfma_f32_16x16x32_bf16 v[30:33], v[166:169], v[214:217], v[30:33]
	v_mfma_f32_16x16x32_bf16 v[22:25], v[174:177], v[214:217], v[22:25]
	v_mfma_f32_16x16x32_bf16 v[14:17], v[166:169], v[222:225], v[14:17]
	v_mfma_f32_16x16x32_bf16 v[6:9], v[174:177], v[222:225], v[6:9]
	v_mfma_f32_16x16x32_bf16 v[62:65], v[170:173], v[202:205], v[62:65]
	v_mfma_f32_16x16x32_bf16 v[54:57], v[178:181], v[202:205], v[54:57]
	v_mfma_f32_16x16x32_bf16 v[46:49], v[170:173], v[210:213], v[46:49]
	v_mfma_f32_16x16x32_bf16 v[38:41], v[178:181], v[210:213], v[38:41]
	v_mfma_f32_16x16x32_bf16 v[30:33], v[170:173], v[218:221], v[30:33]
	v_mfma_f32_16x16x32_bf16 v[22:25], v[178:181], v[218:221], v[22:25]
	v_mfma_f32_16x16x32_bf16 v[14:17], v[170:173], v[226:229], v[14:17]
	v_mfma_f32_16x16x32_bf16 v[6:9], v[178:181], v[226:229], v[6:9]
	s_setprio 0
	s_setprio 1
	v_mfma_f32_16x16x32_bf16 v[58:61], v[182:185], v[198:201], v[58:61]
	v_mfma_f32_16x16x32_bf16 v[50:53], v[190:193], v[198:201], v[50:53]
	v_mfma_f32_16x16x32_bf16 v[42:45], v[182:185], v[206:209], v[42:45]
	v_mfma_f32_16x16x32_bf16 v[34:37], v[190:193], v[206:209], v[34:37]
	v_mfma_f32_16x16x32_bf16 v[26:29], v[182:185], v[214:217], v[26:29]
	v_mfma_f32_16x16x32_bf16 v[18:21], v[190:193], v[214:217], v[18:21]
	v_mfma_f32_16x16x32_bf16 v[10:13], v[182:185], v[222:225], v[10:13]
	v_mfma_f32_16x16x32_bf16 v[2:5], v[190:193], v[222:225], v[2:5]
	v_mfma_f32_16x16x32_bf16 v[58:61], v[186:189], v[202:205], v[58:61]
	v_mfma_f32_16x16x32_bf16 v[50:53], v[194:197], v[202:205], v[50:53]
	v_mfma_f32_16x16x32_bf16 v[42:45], v[186:189], v[210:213], v[42:45]
	v_mfma_f32_16x16x32_bf16 v[34:37], v[194:197], v[210:213], v[34:37]
	v_mfma_f32_16x16x32_bf16 v[26:29], v[186:189], v[218:221], v[26:29]
	v_mfma_f32_16x16x32_bf16 v[18:21], v[194:197], v[218:221], v[18:21]
	v_mfma_f32_16x16x32_bf16 v[10:13], v[186:189], v[226:229], v[10:13]
	v_mfma_f32_16x16x32_bf16 v[2:5], v[194:197], v[226:229], v[2:5]
.Lms_1:
	s_setprio 0
	s_barrier
	s_add_i32 s45, 0, 0x18000
	v_add_u32_e32 v138, s45, v155
	s_add_i32 s46, 0, 0x1c000
	ds_read_b128 v[166:169], v138
	ds_read_b128 v[170:173], v138 offset:1024
	ds_read_b128 v[174:177], v138 offset:2048
	ds_read_b128 v[178:181], v138 offset:3072
	v_add_u32_e32 v138, s46, v155
	ds_read_b128 v[182:185], v138
	ds_read_b128 v[186:189], v138 offset:1024
	ds_read_b128 v[190:193], v138 offset:2048
	ds_read_b128 v[194:197], v138 offset:3072
	s_mov_b32 m0, s66
	ds_read_b128 v[198:201], v159 offset:32768
	ds_read_b128 v[202:205], v159 offset:33792
	ds_read_b128 v[206:209], v159 offset:34816
	ds_read_b128 v[210:213], v159 offset:35840
	ds_read_b128 v[214:217], v159 offset:36864
	ds_read_b128 v[218:221], v159 offset:37888
	ds_read_b128 v[222:225], v159 offset:38912
	ds_read_b128 v[226:229], v159 offset:39936
	global_load_lds_dwordx4 v143, s[42:43]
	s_mov_b32 m0, s67
	s_nop 0
	global_load_lds_dwordx4 v147, s[42:43]
	s_waitcnt vmcnt(8)
	s_waitcnt lgkmcnt(0)
	s_barrier
	s_setprio 1
	s_waitcnt lgkmcnt(0)
	v_mfma_f32_16x16x32_bf16 v[126:129], v[166:169], v[198:201], v[126:129]
	v_mfma_f32_16x16x32_bf16 v[118:121], v[174:177], v[198:201], v[118:121]
	v_mfma_f32_16x16x32_bf16 v[110:113], v[166:169], v[206:209], v[110:113]
	v_mfma_f32_16x16x32_bf16 v[102:105], v[174:177], v[206:209], v[102:105]
	v_mfma_f32_16x16x32_bf16 v[94:97], v[166:169], v[214:217], v[94:97]
	v_mfma_f32_16x16x32_bf16 v[86:89], v[174:177], v[214:217], v[86:89]
	v_mfma_f32_16x16x32_bf16 v[78:81], v[166:169], v[222:225], v[78:81]
	v_mfma_f32_16x16x32_bf16 v[70:73], v[174:177], v[222:225], v[70:73]
	v_mfma_f32_16x16x32_bf16 v[126:129], v[170:173], v[202:205], v[126:129]
	v_mfma_f32_16x16x32_bf16 v[118:121], v[178:181], v[202:205], v[118:121]
	v_mfma_f32_16x16x32_bf16 v[110:113], v[170:173], v[210:213], v[110:113]
	v_mfma_f32_16x16x32_bf16 v[102:105], v[178:181], v[210:213], v[102:105]
	v_mfma_f32_16x16x32_bf16 v[94:97], v[170:173], v[218:221], v[94:97]
	v_mfma_f32_16x16x32_bf16 v[86:89], v[178:181], v[218:221], v[86:89]
	v_mfma_f32_16x16x32_bf16 v[78:81], v[170:173], v[226:229], v[78:81]
	v_mfma_f32_16x16x32_bf16 v[70:73], v[178:181], v[226:229], v[70:73]
	s_setprio 0
	s_setprio 1
	v_mfma_f32_16x16x32_bf16 v[122:125], v[182:185], v[198:201], v[122:125]
	v_mfma_f32_16x16x32_bf16 v[114:117], v[190:193], v[198:201], v[114:117]
	v_mfma_f32_16x16x32_bf16 v[106:109], v[182:185], v[206:209], v[106:109]
	v_mfma_f32_16x16x32_bf16 v[98:101], v[190:193], v[206:209], v[98:101]
	v_mfma_f32_16x16x32_bf16 v[90:93], v[182:185], v[214:217], v[90:93]
	v_mfma_f32_16x16x32_bf16 v[82:85], v[190:193], v[214:217], v[82:85]
	v_mfma_f32_16x16x32_bf16 v[74:77], v[182:185], v[222:225], v[74:77]
	v_mfma_f32_16x16x32_bf16 v[66:69], v[190:193], v[222:225], v[66:69]
	v_mfma_f32_16x16x32_bf16 v[122:125], v[186:189], v[202:205], v[122:125]
	v_mfma_f32_16x16x32_bf16 v[114:117], v[194:197], v[202:205], v[114:117]
	v_mfma_f32_16x16x32_bf16 v[106:109], v[186:189], v[210:213], v[106:109]
	v_mfma_f32_16x16x32_bf16 v[98:101], v[194:197], v[210:213], v[98:101]
	v_mfma_f32_16x16x32_bf16 v[90:93], v[186:189], v[218:221], v[90:93]
	v_mfma_f32_16x16x32_bf16 v[82:85], v[194:197], v[218:221], v[82:85]
	v_mfma_f32_16x16x32_bf16 v[74:77], v[186:189], v[226:229], v[74:77]
	v_mfma_f32_16x16x32_bf16 v[66:69], v[194:197], v[226:229], v[66:69]
	s_setprio 0
	s_barrier
; #define PG8_STAGE(bufoff, gbase, voff) do { _Pragma("unroll") for (int _i = 0; _i < 2; ++_i) \
;         __builtin_amdgcn_global_load_lds((const unsigned*)((const char*)(gbase) + (voff)[_i]), (PG8_LAS unsigned*)(lds + (bufoff) + ldsw + _i * 8192), 16, 0, 0); } while (0)
; #define PG8_LDA(dst, b, h) do { _Pragma("unroll") for (int m = 0; m < 4; ++m) _Pragma("unroll") for (int k = 0; k < 2; ++k) dst[m][k] = *(const PG8_LAS bf16x8*)(lds + PG8_SA(b, h) + aoff + m * 2048 + k * 1024); } while (0)
; #define PG8_MMA(ai, bj, At, Bt) do { __builtin_amdgcn_s_setprio(1); _Pragma("unroll") for (int m = 0; m < 4; ++m) _Pragma("unroll") for (int n = 0; n < 2; ++n) _Pragma("unroll") for (int k = 0; k < 2; ++k) \
;         acc[ai][bj][m][n] = __builtin_amdgcn_mfma_f32_16x16x32_bf16(Bt[n][k], At[m][k], acc[ai][bj][m][n], 0, 0, 0); __builtin_amdgcn_s_setprio(0); } while (0)
; #define PG8_WAIT_V(n) asm volatile("s_waitcnt vmcnt(" #n ")" ::: "memory")
; #define PG8_WAIT_L(n) asm volatile("s_waitcnt lgkmcnt(" #n ")" ::: "memory")
; #define PG8_BAR __builtin_amdgcn_s_barrier()
; #define PG8_SCHED __builtin_amdgcn_sched_barrier(0)
;     __device__ __forceinline__ void signal(int pm, int lane, int wid) const { if (wid == 0 && lane == 0) (void)xb_add(ctr + 32 * pm, 1u); }
;     __device__ __forceinline__ unsigned poll(const Unit& u) const { return xb_ld(ctr + 32 * u.pm); }
;     __device__ __forceinline__ void spin(const Unit& u) const { while (xb_ld(ctr + 32 * u.pm) < 8u) __builtin_amdgcn_s_sleep(2); }
; template <class Epi, class Sched, bool ALIGN_EPI, bool GATHER = false>
; __device__ __forceinline__ void gemm_phase(PG8_LAS unsigned char* lds, const Gemm g, const Sched& S, const Epi& E) {
;     ...
;             PG8_LDA(At, 1, 1); PG8_STAGE(PG8_SB(1, 0), b3, voffB); PG8_STAGE(PG8_SB(1, 1), b3 + hsB, voffB); PG8_STAGE(PG8_SA(1, 0), a3, o0);
;             PG8_WAIT_V(8); PG8_WAIT_L(0); PG8_BAR; PG8_MMA(1, 0, At, B0); PG8_MMA(1, 1, At, B1); PG8_BAR; PG8_SCHED;
;             if constexpr (Sched::SIGNALS) { if (pend >= 0) { pend2 = pend; pend = -1; } else if (pend2 >= 0) { S.signal(pend2, lane, wid); pend2 = -1; } }
;             if constexpr (Sched::WAITS) { if (wst == 1) { pv = S.poll(nxt); wst = 2; } else if (wst == 2) { wst = 0; if (pv < 8u) S.spin(nxt); } }
	s_add_i32 s42, s45, s63
	v_lshl_add_u64 v[232:233], v[232:233], 0, s[18:19]
	s_mov_b32 m0, s42
	ds_read_b128 v[198:201], v159 offset:49152
	ds_read_b128 v[202:205], v159 offset:50176
	ds_read_b128 v[206:209], v159 offset:51200
	ds_read_b128 v[210:213], v159 offset:52224
	ds_read_b128 v[214:217], v159 offset:53248
	ds_read_b128 v[218:221], v159 offset:54272
	ds_read_b128 v[222:225], v159 offset:55296
	ds_read_b128 v[226:229], v159 offset:56320
	global_load_lds_dwordx4 v[232:233], off
	s_add_i32 m0, s42, 0x2000
	s_add_u32 s40, s40, 0x80080
	v_lshl_add_u64 v[232:233], v[234:235], 0, s[18:19]
	s_addc_u32 s41, s41, 0
	s_add_i32 s42, s46, s63
	global_load_lds_dwordx4 v[232:233], off
	v_lshl_add_u64 v[232:233], s[40:41], 0, v[132:133]
	s_mov_b32 m0, s42
	v_lshl_add_u64 v[230:231], v[230:231], 0, s[18:19]
	global_load_lds_dwordx4 v[232:233], off
	v_lshl_add_u64 v[232:233], s[40:41], 0, v[136:137]
	s_add_i32 m0, s42, 0x2000
	s_nop 0
	global_load_lds_dwordx4 v[232:233], off
	v_lshl_add_u64 v[232:233], v[236:237], 0, s[18:19]
	s_mov_b32 m0, s70
	s_nop 0
	global_load_lds_dwordx4 v[232:233], off
	s_mov_b32 m0, s71
	s_nop 0
	global_load_lds_dwordx4 v[230:231], off
	s_waitcnt vmcnt(8)
	s_waitcnt lgkmcnt(0)
	s_barrier
	s_setprio 1
	s_cmp_lg_u32 s99, 0
	s_cbranch_scc1 .Lms_2
	s_waitcnt lgkmcnt(0)
	v_mfma_f32_16x16x32_bf16 v[62:65], v[166:169], v[198:201], v[62:65]
	v_mfma_f32_16x16x32_bf16 v[54:57], v[174:177], v[198:201], v[54:57]
	v_mfma_f32_16x16x32_bf16 v[46:49], v[166:169], v[206:209], v[46:49]
	v_mfma_f32_16x16x32_bf16 v[38:41], v[174:177], v[206:209], v[38:41]
	v_mfma_f32_16x16x32_bf16 v[30:33], v[166:169], v[214:217], v[30:33]
	v_mfma_f32_16x16x32_bf16 v[22:25], v[174:177], v[214:217], v[22:25]
	v_mfma_f32_16x16x32_bf16 v[14:17], v[166:169], v[222:225], v[14:17]
	v_mfma_f32_16x16x32_bf16 v[6:9], v[174:177], v[222:225], v[6:9]
	v_mfma_f32_16x16x32_bf16 v[62:65], v[170:173], v[202:205], v[62:65]
	v_mfma_f32_16x16x32_bf16 v[54:57], v[178:181], v[202:205], v[54:57]
	v_mfma_f32_16x16x32_bf16 v[46:49], v[170:173], v[210:213], v[46:49]
	v_mfma_f32_16x16x32_bf16 v[38:41], v[178:181], v[210:213], v[38:41]
	v_mfma_f32_16x16x32_bf16 v[30:33], v[170:173], v[218:221], v[30:33]
	v_mfma_f32_16x16x32_bf16 v[22:25], v[178:181], v[218:221], v[22:25]
	v_mfma_f32_16x16x32_bf16 v[14:17], v[170:173], v[226:229], v[14:17]
	v_mfma_f32_16x16x32_bf16 v[6:9], v[178:181], v[226:229], v[6:9]
	s_setprio 0
	s_setprio 1
	v_mfma_f32_16x16x32_bf16 v[58:61], v[182:185], v[198:201], v[58:61]
	v_mfma_f32_16x16x32_bf16 v[50:53], v[190:193], v[198:201], v[50:53]
	v_mfma_f32_16x16x32_bf16 v[42:45], v[182:185], v[206:209], v[42:45]
	v_mfma_f32_16x16x32_bf16 v[34:37], v[190:193], v[206:209], v[34:37]
	v_mfma_f32_16x16x32_bf16 v[26:29], v[182:185], v[214:217], v[26:29]
	v_mfma_f32_16x16x32_bf16 v[18:21], v[190:193], v[214:217], v[18:21]
	v_mfma_f32_16x16x32_bf16 v[10:13], v[182:185], v[222:225], v[10:13]
	v_mfma_f32_16x16x32_bf16 v[2:5], v[190:193], v[222:225], v[2:5]
	v_mfma_f32_16x16x32_bf16 v[58:61], v[186:189], v[202:205], v[58:61]
	v_mfma_f32_16x16x32_bf16 v[50:53], v[194:197], v[202:205], v[50:53]
	v_mfma_f32_16x16x32_bf16 v[42:45], v[186:189], v[210:213], v[42:45]
	v_mfma_f32_16x16x32_bf16 v[34:37], v[194:197], v[210:213], v[34:37]
	v_mfma_f32_16x16x32_bf16 v[26:29], v[186:189], v[218:221], v[26:29]
	v_mfma_f32_16x16x32_bf16 v[18:21], v[194:197], v[218:221], v[18:21]
	v_mfma_f32_16x16x32_bf16 v[10:13], v[186:189], v[226:229], v[10:13]
	v_mfma_f32_16x16x32_bf16 v[2:5], v[194:197], v[226:229], v[2:5]
.Lms_2:
	s_setprio 0
	s_barrier
	s_cmp_gt_i32 s78, -1
	s_cbranch_scc1 .LBB0_892
	s_cmp_gt_i32 s12, -1
	s_cselect_b64 s[40:41], -1, 0
	s_and_b64 s[42:43], s[40:41], s[2:3]
	s_and_saveexec_b64 s[40:41], s[42:43]
	s_cbranch_execz .LBB0_887
	s_lshl_b32 s12, s12, 5
	s_lshl_b64 s[42:43], s[12:13], 2
	s_add_u32 s42, s68, s42
	s_addc_u32 s43, s69, s43
	global_atomic_add v139, v1, s[42:43]
	s_branch .LBB0_887

;     __device__ __forceinline__ bool get(int i, int& pm, int& pn) const { return map((long)i * G + c, pm, pn); }
;     __device__ __forceinline__ bool next(int i, Unit& o) const { if (i != 0) return false; o = u; return true; }
;     __device__ __forceinline__ bool next(int i, Unit& u) const { int pm, pn;
;         if (GATHER) { if (!o.get(i, pm, pn)) return false; }
;         else { const bool light = o.c >= rem; const long L = (light && i < 2) ? (long)i * nl + (o.c - rem) : 2L * nl + (long)(light ? i - 2 : i) * o.G + o.c; if (!o.map(L, pm, pn)) return false; }
;         const int e = __builtin_amdgcn_readfirstlane(texp[pm]);
;         u.pm = pm; u.pn = pn; u.aux = e; u.kt = KT; u.ui = i; u.rb = (pm - __builtin_amdgcn_readfirstlane(tbase[e])) * 256; u.cn = __builtin_amdgcn_readfirstlane(tcnt[e]);
;         u.A = GATHER ? A : A + (size_t)((unsigned)pm * AT); u.B = B + (size_t)((unsigned)e * BE + (unsigned)pn * BT); return true; }
.LBB0_963:
	s_or_b64 exec, exec, s[6:7]
	s_add_u32 s11, s14, 0x59000000
	s_addc_u32 s38, s15, 0
	s_add_u32 s39, s14, 0x21800000
	s_waitcnt vmcnt(0)
	v_mov_b32_e32 v1, v0
	v_cndmask_b32_e64 v2, 0, 1, s[2:3]
	s_addc_u32 s40, s15, 0
	s_waitcnt lgkmcnt(0)
	s_barrier
	v_cmp_ne_u32_e64 s[4:5], 1, v2
	s_andn2_b64 vcc, exec, s[2:3]
	v_readfirstlane_b32 s18, v1
	s_cbranch_vccnz .LBB0_965
	s_ashr_i32 s2, s16, 31
	s_lshr_b32 s2, s2, 29
	s_add_i32 s2, s16, s2
	s_ashr_i32 s3, s2, 3
	s_and_b32 s2, s2, -8
	s_sub_i32 s2, s16, s2
	s_cmp_lt_i32 s2, 0
	s_cselect_b32 s6, s48, s33
	s_mul_i32 s6, s6, s2
	s_ashr_i32 s7, s6, 31
	s_lshr_b32 s7, s7, 26
	s_add_i32 s7, s6, s7
	s_andn2_b32 s7, s7, 63
	s_lshr_b32 s2, s2, 31
	s_sub_i32 s7, s6, s7
	s_add_i32 s2, s2, s33
	s_sub_i32 s16, 64, s7
	s_sub_i32 s7, 0, s7
	s_cmp_lt_u32 s16, 64
	s_cselect_b32 s7, s16, s7
	s_add_i32 s16, s7, s3
	s_cmp_ge_i32 s16, s2
	s_cselect_b32 s17, s2, 0
	s_sub_i32 s16, s16, s17
	s_cmp_lt_i32 s7, s2
	s_cselect_b32 s2, s16, s3
	s_add_i32 s2, s2, s6
	s_ashr_i32 s3, s2, 31
	s_lshr_b32 s3, s3, 26
	s_add_i32 s3, s2, s3
	s_ashr_i32 s6, s3, 6
	s_lshl_b32 s6, s6, 3
	s_sub_i32 s7, s33, s6
	s_min_i32 s7, s7, 8
	s_abs_i32 s16, s7
	v_cvt_f32_u32_e32 v2, s16
	s_sub_i32 s19, 0, s16
	s_andn2_b32 s3, s3, 63
	s_sub_i32 s2, s2, s3
	v_rcp_iflag_f32_e32 v2, v2
	s_abs_i32 s17, s2
	s_xor_b32 s3, s2, s7
	s_ashr_i32 s3, s3, 31
	v_mul_f32_e32 v2, 0x4f7ffffe, v2
	v_cvt_u32_f32_e32 v2, v2
	s_nop 0
	v_readfirstlane_b32 s20, v2
	s_mul_i32 s19, s19, s20
	s_mul_hi_u32 s19, s20, s19
	s_add_i32 s20, s20, s19
	s_mul_hi_u32 s19, s17, s20
	s_mul_i32 s20, s19, s16
	s_sub_i32 s17, s17, s20
	s_add_i32 s20, s19, 1
	s_sub_i32 s21, s17, s16
	s_cmp_ge_u32 s17, s16
	s_cselect_b32 s19, s20, s19
	s_cselect_b32 s17, s21, s17
	s_add_i32 s20, s19, 1
	s_cmp_ge_u32 s17, s16
	s_cselect_b32 s16, s20, s19
	s_xor_b32 s16, s16, s3
	s_sub_i32 s64, s16, s3
	s_mul_i32 s3, s64, s7
	s_sub_i32 s2, s2, s3
	s_add_i32 s2, s2, s6
	s_lshl_b32 s3, s2, 2
	s_add_i32 s3, s3, 0
	s_add_i32 s3, s3, 0x20240
	v_mov_b32_e32 v2, s3
	ds_read_b32 v2, v2
	s_lshl_b32 s3, s2, 19
	s_add_u32 s26, s11, s3
	s_addc_u32 s27, s38, 0
	s_waitcnt lgkmcnt(0)
	v_readfirstlane_b32 s6, v2
	s_lshl_b32 s98, s6, 2
	v_mov_b32_e32 v251, s98
	v_add_u32_e32 v251, 0x20100, v251
	ds_read_b32 v252, v251
	ds_read_b32 v253, v251 offset:128
	s_waitcnt lgkmcnt(0)
	v_readfirstlane_b32 s98, v252
	v_readfirstlane_b32 s100, v253
	s_nop 3
	s_sub_i32 s100, s2, s100
	s_lshl_b32 s100, s100, 8
	s_sub_i32 s98, s98, s100
	s_cmp_le_i32 s98, 128
	s_cselect_b32 s98, 1, 0
	s_lshl_b32 s3, s6, 22
	s_lshl_b32 s6, s64, 19
	s_add_i32 s3, s3, s6
	s_add_u32 s28, s39, s3
	s_addc_u32 s29, s40, 0
	s_lshl_b32 s2, s2, 5
	s_ashr_i32 s3, s2, 31
	s_and_b64 vcc, exec, s[4:5]
	s_cbranch_vccz .LBB0_966
	s_branch .LBB0_1015

;     __device__ __forceinline__ bool next(int i, Unit& o) const { if (i != 0) return false; o = u; return true; }
; template <class Epi, class Sched, bool ALIGN_EPI, bool GATHER = false>
; __device__ __forceinline__ void gemm_phase(PG8_LAS unsigned char* lds, const Gemm g, const Sched& S, const Epi& E) {
;     ...
;     for (;;) {
;         const bool has_next = S.next(ui + 1, nxt);
;         if constexpr (Sched::WAITS) wst = has_next ? 1 : 0;
;         const char* nA = has_next ? nxt.A : cA; const char* nB = has_next ? nxt.B : cB;
.LBB0_973:
	s_mov_b32 s99, s98
	s_add_i32 s60, s20, 1
	s_cmp_lg_u32 s20, 0
	s_cselect_b64 s[22:23], -1, 0
	s_or_b64 s[22:23], s[8:9], s[22:23]
	s_mov_b64 s[2:3], -1
	s_and_b64 vcc, exec, s[22:23]
	s_cbranch_vccz .LBB0_975
	s_add_i32 s20, s20, -1
	s_and_b64 s[2:3], s[18:19], exec
	s_cselect_b32 s2, s20, s60
	s_mul_hi_i32 s3, s2, s10
	s_mul_i32 s2, s2, s10
	s_add_u32 s30, s2, s42
	s_addc_u32 s31, s3, s43
	s_mov_b64 s[2:3], 0

;     __device__ __forceinline__ bool get(int i, int& pm, int& pn) const { return map((long)i * G + c, pm, pn); }
;     __device__ __forceinline__ bool next(int i, Unit& o) const { if (i != 0) return false; o = u; return true; }
;     __device__ __forceinline__ bool map(long L, int& pm, int& pn) const {
;         if (L >= nwg) return false;
;         const int nig = WGM * nN;
;         int wgid = (int)L; { const int q = nwg / NXCD, r = nwg % NXCD, xcd = wgid % NXCD; int off = wgid / NXCD; const int cs = (xcd < r ? xcd * (q + 1) : r * (q + 1) + (xcd - r) * q), len = q + (xcd < r ? 1 : 0);
;             if (rot) { const int lead = (nig - cs % nig) % nig; if (lead < len) { off += lead; if (off >= len) off -= len; } }
;             wgid = cs + off; }
;         const int gid = wgid / nig, fm = gid * WGM, gsz = (nM - fm) < WGM ? (nM - fm) : WGM;
;         pm = fm + ((wgid % nig) % gsz); pn = (wgid % nig) / gsz; return true;
;     __device__ __forceinline__ bool next(int i, Unit& u) const { int pm, pn;
;         if (GATHER) { if (!o.get(i, pm, pn)) return false; }
;         else { const bool light = o.c >= rem; const long L = (light && i < 2) ? (long)i * nl + (o.c - rem) : 2L * nl + (long)(light ? i - 2 : i) * o.G + o.c; if (!o.map(L, pm, pn)) return false; }
;         const int e = __builtin_amdgcn_readfirstlane(texp[pm]);
;         u.pm = pm; u.pn = pn; u.aux = e; u.kt = KT; u.ui = i; u.rb = (pm - __builtin_amdgcn_readfirstlane(tbase[e])) * 256; u.cn = __builtin_amdgcn_readfirstlane(tcnt[e]);
;         u.A = GATHER ? A : A + (size_t)((unsigned)pm * AT); u.B = B + (size_t)((unsigned)e * BE + (unsigned)pn * BT); return true; }
.LBB0_977:
	v_cmp_ge_i64_e32 vcc, s[30:31], v[142:143]
	v_cmp_lt_i64_e64 s[2:3], s[30:31], v[142:143]
	s_mov_b64 s[24:25], s[28:29]
	s_mov_b64 s[20:21], s[26:27]
	s_cbranch_vccnz .LBB0_979
	s_ashr_i32 s20, s30, 31
	s_lshr_b32 s20, s20, 29
	s_add_i32 s20, s30, s20
	s_ashr_i32 s21, s20, 3
	s_and_b32 s20, s20, -8
	s_sub_i32 s20, s30, s20
	s_cmp_lt_i32 s20, 0
	s_cselect_b32 s22, s48, s33
	s_mul_i32 s22, s22, s20
	s_ashr_i32 s23, s22, 31
	s_lshr_b32 s23, s23, 26
	s_add_i32 s23, s22, s23
	s_andn2_b32 s23, s23, 63
	s_lshr_b32 s20, s20, 31
	s_sub_i32 s23, s22, s23
	s_add_i32 s20, s20, s33
	s_sub_i32 s24, 64, s23
	s_sub_i32 s23, 0, s23
	s_cmp_lt_u32 s24, 64
	s_cselect_b32 s23, s24, s23
	s_add_i32 s24, s23, s21
	s_cmp_ge_i32 s24, s20
	s_cselect_b32 s25, s20, 0
	s_sub_i32 s24, s24, s25
	s_cmp_lt_i32 s23, s20
	s_cselect_b32 s20, s24, s21
	s_add_i32 s20, s20, s22
	s_ashr_i32 s21, s20, 31
	s_lshr_b32 s21, s21, 26
	s_add_i32 s21, s20, s21
	s_ashr_i32 s22, s21, 6
	s_lshl_b32 s22, s22, 3
	s_sub_i32 s23, s33, s22
	s_min_i32 s23, s23, 8
	s_abs_i32 s24, s23
	v_cvt_f32_u32_e32 v2, s24
	s_sub_i32 s30, 0, s24
	s_andn2_b32 s21, s21, 63
	s_sub_i32 s20, s20, s21
	v_rcp_iflag_f32_e32 v2, v2
	s_abs_i32 s25, s20
	s_xor_b32 s21, s20, s23
	s_ashr_i32 s21, s21, 31
	v_mul_f32_e32 v2, 0x4f7ffffe, v2
	v_cvt_u32_f32_e32 v2, v2
	s_mov_b32 s63, s60
	v_readfirstlane_b32 s31, v2
	s_mul_i32 s30, s30, s31
	s_mul_hi_u32 s30, s31, s30
	s_add_i32 s31, s31, s30
	s_mul_hi_u32 s30, s25, s31
	s_mul_i32 s31, s30, s24
	s_sub_i32 s25, s25, s31
	s_add_i32 s31, s30, 1
	s_sub_i32 s34, s25, s24
	s_cmp_ge_u32 s25, s24
	s_cselect_b32 s30, s31, s30
	s_cselect_b32 s25, s34, s25
	s_add_i32 s31, s30, 1
	s_cmp_ge_u32 s25, s24
	s_cselect_b32 s24, s31, s30
	s_xor_b32 s24, s24, s21
	s_sub_i32 s61, s24, s21
	s_mul_i32 s21, s61, s23
	s_sub_i32 s20, s20, s21
	s_add_i32 s62, s20, s22
	s_lshl_b32 s20, s62, 2
	s_add_i32 s20, s20, 0
	s_add_i32 s20, s20, 0x20240
	v_mov_b32_e32 v2, s20
	ds_read_b32 v2, v2
	s_lshl_b32 s20, s62, 19
	s_add_u32 s20, s11, s20
	s_addc_u32 s21, s38, 0
	s_lshl_b32 s23, s61, 19
	s_waitcnt lgkmcnt(0)
	v_readfirstlane_b32 s22, v2
	s_lshl_b32 s98, s22, 2
	v_mov_b32_e32 v251, s98
	v_add_u32_e32 v251, 0x20100, v251
	ds_read_b32 v252, v251
	ds_read_b32 v253, v251 offset:128
	s_waitcnt lgkmcnt(0)
	v_readfirstlane_b32 s98, v252
	v_readfirstlane_b32 s100, v253
	s_nop 3
	s_sub_i32 s100, s62, s100
	s_lshl_b32 s100, s100, 8
	s_sub_i32 s98, s98, s100
	s_cmp_le_i32 s98, 128
	s_cselect_b32 s98, 1, 0
	s_lshl_b32 s22, s22, 22
	s_add_i32 s22, s22, s23
	s_add_u32 s24, s39, s22
	s_addc_u32 s25, s40, 0

; #define PG8_STAGE(bufoff, gbase, voff) do { _Pragma("unroll") for (int _i = 0; _i < 2; ++_i) \
;         __builtin_amdgcn_global_load_lds((const unsigned*)((const char*)(gbase) + (voff)[_i]), (PG8_LAS unsigned*)(lds + (bufoff) + ldsw + _i * 8192), 16, 0, 0); } while (0)
; #define PG8_LDA(dst, b, h) do { _Pragma("unroll") for (int m = 0; m < 4; ++m) _Pragma("unroll") for (int k = 0; k < 2; ++k) dst[m][k] = *(const PG8_LAS bf16x8*)(lds + PG8_SA(b, h) + aoff + m * 2048 + k * 1024); } while (0)
; #define PG8_LDB(dst, b, h) do { _Pragma("unroll") for (int n = 0; n < 2; ++n) _Pragma("unroll") for (int k = 0; k < 2; ++k) dst[n][k] = *(const PG8_LAS bf16x8*)(lds + PG8_SB(b, h) + boff + n * 2048 + k * 1024); } while (0)
; #define PG8_MMA(ai, bj, At, Bt) do { __builtin_amdgcn_s_setprio(1); _Pragma("unroll") for (int m = 0; m < 4; ++m) _Pragma("unroll") for (int n = 0; n < 2; ++n) _Pragma("unroll") for (int k = 0; k < 2; ++k) \
;         acc[ai][bj][m][n] = __builtin_amdgcn_mfma_f32_16x16x32_bf16(Bt[n][k], At[m][k], acc[ai][bj][m][n], 0, 0, 0); __builtin_amdgcn_s_setprio(0); } while (0)
; #define PG8_WAIT_V(n) asm volatile("s_waitcnt vmcnt(" #n ")" ::: "memory")
; #define PG8_WAIT_L(n) asm volatile("s_waitcnt lgkmcnt(" #n ")" ::: "memory")
; #define PG8_BAR __builtin_amdgcn_s_barrier()
; #define PG8_SCHED __builtin_amdgcn_sched_barrier(0)
; template <class Epi, class Sched, bool ALIGN_EPI, bool GATHER = false>
; __device__ __forceinline__ void gemm_phase(PG8_LAS unsigned char* lds, const Gemm g, const Sched& S, const Epi& E) {
;     ...
;             PG8_LDB(B0, 0, 0); PG8_LDB(B1, 0, 1); PG8_SCHED; PG8_LDA(At, 0, 0); PG8_STAGE(PG8_SA(1, 1), a1, vc[1]);
;             PG8_WAIT_V(8); PG8_WAIT_L(0); PG8_BAR; PG8_MMA(0, 0, At, B0); PG8_MMA(0, 1, At, B1); PG8_BAR; PG8_SCHED;
;             PG8_LDA(At, 0, 1); PG8_STAGE(PG8_SB(0, 0), b2, voffB); PG8_STAGE(PG8_SB(0, 1), b2 + hsB, voffB); PG8_STAGE(PG8_SA(0, 0), a2, o0);
;             PG8_WAIT_V(8); PG8_WAIT_L(0); PG8_BAR; PG8_MMA(1, 0, At, B0); PG8_MMA(1, 1, At, B1); PG8_BAR; PG8_SCHED;
.LBB0_980:
	ds_read_b128 v[154:157], v151
	ds_read_b128 v[158:161], v151 offset:1024
	ds_read_b128 v[162:165], v151 offset:2048
	ds_read_b128 v[166:169], v151 offset:3072
	ds_read_b128 v[170:173], v152
	ds_read_b128 v[174:177], v152 offset:1024
	ds_read_b128 v[178:181], v152 offset:2048
	ds_read_b128 v[182:185], v152 offset:3072
	s_lshl_b32 s34, s22, 7
	s_add_u32 s68, s26, s34
	s_addc_u32 s69, s27, 0
	s_add_i32 s66, s22, 2
	s_lshl_b32 s34, s66, 7
	s_add_u32 s35, s26, s34
	s_addc_u32 s36, s27, 0
	s_add_u32 s34, s28, s34
	s_addc_u32 s67, s29, 0
	s_cmp_eq_u32 s22, 14
	s_cselect_b32 s37, s21, s36
	s_cselect_b32 s36, s20, s35
	s_cselect_b32 s35, s25, s67
	s_cselect_b32 s34, s24, s34
	v_lshl_add_u64 v[146:147], s[68:69], 0, v[134:135]
	v_lshl_add_u64 v[146:147], v[146:147], 0, s[14:15]
	s_add_i32 m0, s47, 0xc000
	ds_read_b128 v[186:189], v153
	ds_read_b128 v[190:193], v153 offset:1024
	ds_read_b128 v[194:197], v153 offset:2048
	ds_read_b128 v[198:201], v153 offset:3072
	ds_read_b128 v[202:205], v153 offset:4096
	ds_read_b128 v[206:209], v153 offset:5120
	ds_read_b128 v[210:213], v153 offset:6144
	ds_read_b128 v[214:217], v153 offset:7168
	global_load_lds_dwordx4 v[146:147], off
	v_lshl_add_u64 v[146:147], s[68:69], 0, v[138:139]
	v_lshl_add_u64 v[146:147], v[146:147], 0, s[14:15]
	s_add_i32 m0, s47, 0xe000
	s_nop 0
	global_load_lds_dwordx4 v[146:147], off
	s_waitcnt vmcnt(8)
	s_waitcnt lgkmcnt(0)
	s_barrier
	s_setprio 1
	s_waitcnt lgkmcnt(0)
	v_mfma_f32_16x16x32_bf16 v[126:129], v[154:157], v[186:189], v[126:129]
	v_mfma_f32_16x16x32_bf16 v[122:125], v[162:165], v[186:189], v[122:125]
	v_mfma_f32_16x16x32_bf16 v[110:113], v[154:157], v[194:197], v[110:113]
	v_mfma_f32_16x16x32_bf16 v[106:109], v[162:165], v[194:197], v[106:109]
	v_mfma_f32_16x16x32_bf16 v[94:97], v[154:157], v[202:205], v[94:97]
	v_mfma_f32_16x16x32_bf16 v[90:93], v[162:165], v[202:205], v[90:93]
	v_mfma_f32_16x16x32_bf16 v[78:81], v[154:157], v[210:213], v[78:81]
	v_mfma_f32_16x16x32_bf16 v[74:77], v[162:165], v[210:213], v[74:77]
	v_mfma_f32_16x16x32_bf16 v[126:129], v[158:161], v[190:193], v[126:129]
	v_mfma_f32_16x16x32_bf16 v[122:125], v[166:169], v[190:193], v[122:125]
	v_mfma_f32_16x16x32_bf16 v[110:113], v[158:161], v[198:201], v[110:113]
	v_mfma_f32_16x16x32_bf16 v[106:109], v[166:169], v[198:201], v[106:109]
	v_mfma_f32_16x16x32_bf16 v[94:97], v[158:161], v[206:209], v[94:97]
	v_mfma_f32_16x16x32_bf16 v[90:93], v[166:169], v[206:209], v[90:93]
	v_mfma_f32_16x16x32_bf16 v[78:81], v[158:161], v[214:217], v[78:81]
	v_mfma_f32_16x16x32_bf16 v[74:77], v[166:169], v[214:217], v[74:77]
	s_setprio 0
	s_setprio 1
	v_mfma_f32_16x16x32_bf16 v[118:121], v[170:173], v[186:189], v[118:121]
	v_mfma_f32_16x16x32_bf16 v[114:117], v[178:181], v[186:189], v[114:117]
	v_mfma_f32_16x16x32_bf16 v[102:105], v[170:173], v[194:197], v[102:105]
	v_mfma_f32_16x16x32_bf16 v[98:101], v[178:181], v[194:197], v[98:101]
	v_mfma_f32_16x16x32_bf16 v[86:89], v[170:173], v[202:205], v[86:89]
	v_mfma_f32_16x16x32_bf16 v[82:85], v[178:181], v[202:205], v[82:85]
	v_mfma_f32_16x16x32_bf16 v[70:73], v[170:173], v[210:213], v[70:73]
	v_mfma_f32_16x16x32_bf16 v[66:69], v[178:181], v[210:213], v[66:69]
	v_mfma_f32_16x16x32_bf16 v[118:121], v[174:177], v[190:193], v[118:121]
	v_mfma_f32_16x16x32_bf16 v[114:117], v[182:185], v[190:193], v[114:117]
	v_mfma_f32_16x16x32_bf16 v[102:105], v[174:177], v[198:201], v[102:105]
	v_mfma_f32_16x16x32_bf16 v[98:101], v[182:185], v[198:201], v[98:101]
	v_mfma_f32_16x16x32_bf16 v[86:89], v[174:177], v[206:209], v[86:89]
	v_mfma_f32_16x16x32_bf16 v[82:85], v[182:185], v[206:209], v[82:85]
	v_mfma_f32_16x16x32_bf16 v[70:73], v[174:177], v[214:217], v[70:73]
	v_mfma_f32_16x16x32_bf16 v[66:69], v[182:185], v[214:217], v[66:69]
	s_setprio 0
	s_barrier
	s_add_i32 s67, s58, s46
	v_lshl_add_u64 v[146:147], s[34:35], 0, v[130:131]
	s_mov_b32 m0, s67
	ds_read_b128 v[186:189], v153 offset:16384
	ds_read_b128 v[190:193], v153 offset:17408
	ds_read_b128 v[194:197], v153 offset:18432
	ds_read_b128 v[198:201], v153 offset:19456
	ds_read_b128 v[202:205], v153 offset:20480
	ds_read_b128 v[206:209], v153 offset:21504
	ds_read_b128 v[210:213], v153 offset:22528
	ds_read_b128 v[214:217], v153 offset:23552
	global_load_lds_dwordx4 v[146:147], off
	s_add_i32 m0, s67, 0x2000
	s_add_u32 s68, s34, 0x40000
	v_lshl_add_u64 v[218:219], s[34:35], 0, v[140:141]
	s_addc_u32 s69, s35, 0
	s_add_i32 s67, s59, s46
	global_load_lds_dwordx4 v[218:219], off
	v_lshl_add_u64 v[220:221], s[68:69], 0, v[130:131]
	s_mov_b32 m0, s67
	v_lshl_add_u64 v[222:223], s[36:37], 0, v[136:137]
	global_load_lds_dwordx4 v[220:221], off
	v_lshl_add_u64 v[220:221], s[68:69], 0, v[140:141]
	s_add_i32 m0, s67, 0x2000
	s_nop 0
	global_load_lds_dwordx4 v[220:221], off
	v_lshl_add_u64 v[220:221], s[36:37], 0, v[132:133]
	s_mov_b32 m0, s47
	s_nop 0
	global_load_lds_dwordx4 v[220:221], off
	s_mov_b32 m0, s49
	s_nop 0
	global_load_lds_dwordx4 v[222:223], off
	s_waitcnt vmcnt(8)
	s_waitcnt lgkmcnt(0)
	s_barrier
	s_setprio 1
	s_cmp_lg_u32 s99, 0
	s_cbranch_scc1 .Lms_3
; #define PG8_STAGE(bufoff, gbase, voff) do { _Pragma("unroll") for (int _i = 0; _i < 2; ++_i) \
;         __builtin_amdgcn_global_load_lds((const unsigned*)((const char*)(gbase) + (voff)[_i]), (PG8_LAS unsigned*)(lds + (bufoff) + ldsw + _i * 8192), 16, 0, 0); } while (0)
; #define PG8_LDA(dst, b, h) do { _Pragma("unroll") for (int m = 0; m < 4; ++m) _Pragma("unroll") for (int k = 0; k < 2; ++k) dst[m][k] = *(const PG8_LAS bf16x8*)(lds + PG8_SA(b, h) + aoff + m * 2048 + k * 1024); } while (0)
; #define PG8_LDB(dst, b, h) do { _Pragma("unroll") for (int n = 0; n < 2; ++n) _Pragma("unroll") for (int k = 0; k < 2; ++k) dst[n][k] = *(const PG8_LAS bf16x8*)(lds + PG8_SB(b, h) + boff + n * 2048 + k * 1024); } while (0)
; #define PG8_MMA(ai, bj, At, Bt) do { __builtin_amdgcn_s_setprio(1); _Pragma("unroll") for (int m = 0; m < 4; ++m) _Pragma("unroll") for (int n = 0; n < 2; ++n) _Pragma("unroll") for (int k = 0; k < 2; ++k) \
;         acc[ai][bj][m][n] = __builtin_amdgcn_mfma_f32_16x16x32_bf16(Bt[n][k], At[m][k], acc[ai][bj][m][n], 0, 0, 0); __builtin_amdgcn_s_setprio(0); } while (0)
; #define PG8_WAIT_V(n) asm volatile("s_waitcnt vmcnt(" #n ")" ::: "memory")
; #define PG8_WAIT_L(n) asm volatile("s_waitcnt lgkmcnt(" #n ")" ::: "memory")
; #define PG8_BAR __builtin_amdgcn_s_barrier()
; #define PG8_SCHED __builtin_amdgcn_sched_barrier(0)
; template <class Epi, class Sched, bool ALIGN_EPI, bool GATHER = false>
; __device__ __forceinline__ void gemm_phase(PG8_LAS unsigned char* lds, const Gemm g, const Sched& S, const Epi& E) {
;     ...
;             PG8_WAIT_V(8); PG8_WAIT_L(0); PG8_BAR; PG8_MMA(1, 0, At, B0); PG8_MMA(1, 1, At, B1); PG8_BAR; PG8_SCHED;
;             PG8_LDB(B0, 1, 0); PG8_LDB(B1, 1, 1); PG8_SCHED; PG8_LDA(At, 1, 0); PG8_STAGE(PG8_SA(0, 1), a2, o1);
;             PG8_WAIT_V(8); PG8_WAIT_L(0); PG8_BAR; PG8_MMA(0, 0, At, B0); PG8_MMA(0, 1, At, B1); PG8_BAR; PG8_SCHED;
	s_waitcnt lgkmcnt(0)
	v_mfma_f32_16x16x32_bf16 v[62:65], v[154:157], v[186:189], v[62:65]
	v_mfma_f32_16x16x32_bf16 v[58:61], v[162:165], v[186:189], v[58:61]
	v_mfma_f32_16x16x32_bf16 v[46:49], v[154:157], v[194:197], v[46:49]
	v_mfma_f32_16x16x32_bf16 v[42:45], v[162:165], v[194:197], v[42:45]
	v_mfma_f32_16x16x32_bf16 v[14:17], v[154:157], v[202:205], v[14:17]
	v_mfma_f32_16x16x32_bf16 v[10:13], v[162:165], v[202:205], v[10:13]
	v_mfma_f32_16x16x32_bf16 v[6:9], v[154:157], v[210:213], v[6:9]
	v_mfma_f32_16x16x32_bf16 v[2:5], v[162:165], v[210:213], v[2:5]
	v_mfma_f32_16x16x32_bf16 v[62:65], v[158:161], v[190:193], v[62:65]
	v_mfma_f32_16x16x32_bf16 v[58:61], v[166:169], v[190:193], v[58:61]
	v_mfma_f32_16x16x32_bf16 v[46:49], v[158:161], v[198:201], v[46:49]
	v_mfma_f32_16x16x32_bf16 v[42:45], v[166:169], v[198:201], v[42:45]
	v_mfma_f32_16x16x32_bf16 v[14:17], v[158:161], v[206:209], v[14:17]
	v_mfma_f32_16x16x32_bf16 v[10:13], v[166:169], v[206:209], v[10:13]
	v_mfma_f32_16x16x32_bf16 v[6:9], v[158:161], v[214:217], v[6:9]
	v_mfma_f32_16x16x32_bf16 v[2:5], v[166:169], v[214:217], v[2:5]
	s_setprio 0
	s_setprio 1
	v_mfma_f32_16x16x32_bf16 v[54:57], v[170:173], v[186:189], v[54:57]
	v_mfma_f32_16x16x32_bf16 v[50:53], v[178:181], v[186:189], v[50:53]
	v_mfma_f32_16x16x32_bf16 v[30:33], v[170:173], v[194:197], v[30:33]
	v_mfma_f32_16x16x32_bf16 v[26:29], v[178:181], v[194:197], v[26:29]
	v_mfma_f32_16x16x32_bf16 v[34:37], v[170:173], v[202:205], v[34:37]
	v_mfma_f32_16x16x32_bf16 v[38:41], v[178:181], v[202:205], v[38:41]
	v_mfma_f32_16x16x32_bf16 v[18:21], v[170:173], v[210:213], v[18:21]
	v_mfma_f32_16x16x32_bf16 v[22:25], v[178:181], v[210:213], v[22:25]
	v_mfma_f32_16x16x32_bf16 v[54:57], v[174:177], v[190:193], v[54:57]
	v_mfma_f32_16x16x32_bf16 v[50:53], v[182:185], v[190:193], v[50:53]
	v_mfma_f32_16x16x32_bf16 v[30:33], v[174:177], v[198:201], v[30:33]
	v_mfma_f32_16x16x32_bf16 v[26:29], v[182:185], v[198:201], v[26:29]
	v_mfma_f32_16x16x32_bf16 v[34:37], v[174:177], v[206:209], v[34:37]
	v_mfma_f32_16x16x32_bf16 v[38:41], v[182:185], v[206:209], v[38:41]
	v_mfma_f32_16x16x32_bf16 v[18:21], v[174:177], v[214:217], v[18:21]
	v_mfma_f32_16x16x32_bf16 v[22:25], v[182:185], v[214:217], v[22:25]
.Lms_3:
	s_setprio 0
	s_barrier
	s_add_i32 s67, 0, 0x18000
	v_add_u32_e32 v144, s67, v1
	s_add_i32 s68, 0, 0x1c000
	ds_read_b128 v[154:157], v144
	ds_read_b128 v[158:161], v144 offset:1024
	ds_read_b128 v[162:165], v144 offset:2048
	ds_read_b128 v[166:169], v144 offset:3072
	v_add_u32_e32 v144, s68, v1
	ds_read_b128 v[170:173], v144
	ds_read_b128 v[174:177], v144 offset:1024
	ds_read_b128 v[178:181], v144 offset:2048
	ds_read_b128 v[182:185], v144 offset:3072
	s_mov_b32 m0, s50
	v_lshl_add_u64 v[224:225], s[36:37], 0, v[134:135]
	ds_read_b128 v[186:189], v153 offset:32768
	ds_read_b128 v[190:193], v153 offset:33792
	ds_read_b128 v[194:197], v153 offset:34816
	ds_read_b128 v[198:201], v153 offset:35840
	ds_read_b128 v[202:205], v153 offset:36864
	ds_read_b128 v[206:209], v153 offset:37888
	ds_read_b128 v[210:213], v153 offset:38912
	ds_read_b128 v[214:217], v153 offset:39936
	global_load_lds_dwordx4 v[224:225], off
	v_lshl_add_u64 v[224:225], s[36:37], 0, v[138:139]
	s_mov_b32 m0, s51
	s_nop 0
	global_load_lds_dwordx4 v[224:225], off
	s_waitcnt vmcnt(8)
	s_waitcnt lgkmcnt(0)
	s_barrier
	s_setprio 1
	s_waitcnt lgkmcnt(0)
	v_mfma_f32_16x16x32_bf16 v[126:129], v[154:157], v[186:189], v[126:129]
	v_mfma_f32_16x16x32_bf16 v[122:125], v[162:165], v[186:189], v[122:125]
	v_mfma_f32_16x16x32_bf16 v[110:113], v[154:157], v[194:197], v[110:113]
	v_mfma_f32_16x16x32_bf16 v[106:109], v[162:165], v[194:197], v[106:109]
	v_mfma_f32_16x16x32_bf16 v[94:97], v[154:157], v[202:205], v[94:97]
	v_mfma_f32_16x16x32_bf16 v[90:93], v[162:165], v[202:205], v[90:93]
	v_mfma_f32_16x16x32_bf16 v[78:81], v[154:157], v[210:213], v[78:81]
	v_mfma_f32_16x16x32_bf16 v[74:77], v[162:165], v[210:213], v[74:77]
	v_mfma_f32_16x16x32_bf16 v[126:129], v[158:161], v[190:193], v[126:129]
	v_mfma_f32_16x16x32_bf16 v[122:125], v[166:169], v[190:193], v[122:125]
	v_mfma_f32_16x16x32_bf16 v[110:113], v[158:161], v[198:201], v[110:113]
	v_mfma_f32_16x16x32_bf16 v[106:109], v[166:169], v[198:201], v[106:109]
	v_mfma_f32_16x16x32_bf16 v[94:97], v[158:161], v[206:209], v[94:97]
	v_mfma_f32_16x16x32_bf16 v[90:93], v[166:169], v[206:209], v[90:93]
	v_mfma_f32_16x16x32_bf16 v[78:81], v[158:161], v[214:217], v[78:81]
	v_mfma_f32_16x16x32_bf16 v[74:77], v[166:169], v[214:217], v[74:77]
	s_setprio 0
	s_setprio 1
	v_mfma_f32_16x16x32_bf16 v[118:121], v[170:173], v[186:189], v[118:121]
	v_mfma_f32_16x16x32_bf16 v[114:117], v[178:181], v[186:189], v[114:117]
	v_mfma_f32_16x16x32_bf16 v[102:105], v[170:173], v[194:197], v[102:105]
	v_mfma_f32_16x16x32_bf16 v[98:101], v[178:181], v[194:197], v[98:101]
	v_mfma_f32_16x16x32_bf16 v[86:89], v[170:173], v[202:205], v[86:89]
	v_mfma_f32_16x16x32_bf16 v[82:85], v[178:181], v[202:205], v[82:85]
	v_mfma_f32_16x16x32_bf16 v[70:73], v[170:173], v[210:213], v[70:73]
	v_mfma_f32_16x16x32_bf16 v[66:69], v[178:181], v[210:213], v[66:69]
	v_mfma_f32_16x16x32_bf16 v[118:121], v[174:177], v[190:193], v[118:121]
	v_mfma_f32_16x16x32_bf16 v[114:117], v[182:185], v[190:193], v[114:117]
	v_mfma_f32_16x16x32_bf16 v[102:105], v[174:177], v[198:201], v[102:105]
	v_mfma_f32_16x16x32_bf16 v[98:101], v[182:185], v[198:201], v[98:101]
	v_mfma_f32_16x16x32_bf16 v[86:89], v[174:177], v[206:209], v[86:89]
	v_mfma_f32_16x16x32_bf16 v[82:85], v[182:185], v[206:209], v[82:85]
	v_mfma_f32_16x16x32_bf16 v[70:73], v[174:177], v[214:217], v[70:73]
	v_mfma_f32_16x16x32_bf16 v[66:69], v[182:185], v[214:217], v[66:69]
	s_setprio 0
	s_barrier
; #define PG8_STAGE(bufoff, gbase, voff) do { _Pragma("unroll") for (int _i = 0; _i < 2; ++_i) \
;         __builtin_amdgcn_global_load_lds((const unsigned*)((const char*)(gbase) + (voff)[_i]), (PG8_LAS unsigned*)(lds + (bufoff) + ldsw + _i * 8192), 16, 0, 0); } while (0)
; #define PG8_LDA(dst, b, h) do { _Pragma("unroll") for (int m = 0; m < 4; ++m) _Pragma("unroll") for (int k = 0; k < 2; ++k) dst[m][k] = *(const PG8_LAS bf16x8*)(lds + PG8_SA(b, h) + aoff + m * 2048 + k * 1024); } while (0)
; #define PG8_MMA(ai, bj, At, Bt) do { __builtin_amdgcn_s_setprio(1); _Pragma("unroll") for (int m = 0; m < 4; ++m) _Pragma("unroll") for (int n = 0; n < 2; ++n) _Pragma("unroll") for (int k = 0; k < 2; ++k) \
;         acc[ai][bj][m][n] = __builtin_amdgcn_mfma_f32_16x16x32_bf16(Bt[n][k], At[m][k], acc[ai][bj][m][n], 0, 0, 0); __builtin_amdgcn_s_setprio(0); } while (0)
; #define PG8_WAIT_V(n) asm volatile("s_waitcnt vmcnt(" #n ")" ::: "memory")
; #define PG8_WAIT_L(n) asm volatile("s_waitcnt lgkmcnt(" #n ")" ::: "memory")
; #define PG8_BAR __builtin_amdgcn_s_barrier()
; #define PG8_SCHED __builtin_amdgcn_sched_barrier(0)
;     __device__ __forceinline__ void signal(int pm, int lane, int wid) const { if (wid == 0 && lane == 0) (void)xb_add(ctr + 32 * pm, 1u); }
;     __device__ __forceinline__ unsigned poll(const Unit& u) const { return xb_ld(ctr + 32 * u.pm); }
;     __device__ __forceinline__ void spin(const Unit& u) const { while (xb_ld(ctr + 32 * u.pm) < 8u) __builtin_amdgcn_s_sleep(2); }
; template <class Epi, class Sched, bool ALIGN_EPI, bool GATHER = false>
; __device__ __forceinline__ void gemm_phase(PG8_LAS unsigned char* lds, const Gemm g, const Sched& S, const Epi& E) {
;     ...
;             PG8_LDA(At, 1, 1); PG8_STAGE(PG8_SB(1, 0), b3, voffB); PG8_STAGE(PG8_SB(1, 1), b3 + hsB, voffB); PG8_STAGE(PG8_SA(1, 0), a3, o0);
;             PG8_WAIT_V(8); PG8_WAIT_L(0); PG8_BAR; PG8_MMA(1, 0, At, B0); PG8_MMA(1, 1, At, B1); PG8_BAR; PG8_SCHED;
;             if constexpr (Sched::SIGNALS) { if (pend >= 0) { pend2 = pend; pend = -1; } else if (pend2 >= 0) { S.signal(pend2, lane, wid); pend2 = -1; } }
;             if constexpr (Sched::WAITS) { if (wst == 1) { pv = S.poll(nxt); wst = 2; } else if (wst == 2) { wst = 0; if (pv < 8u) S.spin(nxt); } }
	s_add_i32 s36, s67, s46
	v_lshl_add_u64 v[146:147], v[146:147], 0, s[14:15]
	s_mov_b32 m0, s36
	ds_read_b128 v[186:189], v153 offset:49152
	ds_read_b128 v[190:193], v153 offset:50176
	ds_read_b128 v[194:197], v153 offset:51200
	ds_read_b128 v[198:201], v153 offset:52224
	ds_read_b128 v[202:205], v153 offset:53248
	ds_read_b128 v[206:209], v153 offset:54272
	ds_read_b128 v[210:213], v153 offset:55296
	ds_read_b128 v[214:217], v153 offset:56320
	global_load_lds_dwordx4 v[146:147], off
	s_add_i32 m0, s36, 0x2000
	s_add_u32 s34, s34, 0x40080
	v_lshl_add_u64 v[146:147], v[218:219], 0, s[14:15]
	s_addc_u32 s35, s35, 0
	s_add_i32 s36, s68, s46
	global_load_lds_dwordx4 v[146:147], off
	v_lshl_add_u64 v[146:147], s[34:35], 0, v[130:131]
	s_mov_b32 m0, s36
	s_nop 0
	global_load_lds_dwordx4 v[146:147], off
	v_lshl_add_u64 v[146:147], s[34:35], 0, v[140:141]
	s_add_i32 m0, s36, 0x2000
	s_nop 0
	global_load_lds_dwordx4 v[146:147], off
	v_lshl_add_u64 v[146:147], v[220:221], 0, s[14:15]
	s_mov_b32 m0, s56
	s_nop 0
	global_load_lds_dwordx4 v[146:147], off
	v_lshl_add_u64 v[146:147], v[222:223], 0, s[14:15]
	s_mov_b32 m0, s57
	s_nop 0
	global_load_lds_dwordx4 v[146:147], off
	s_waitcnt vmcnt(8)
	s_waitcnt lgkmcnt(0)
	s_barrier
	s_setprio 1
	s_cmp_lg_u32 s99, 0
	s_cbranch_scc1 .Lms_4
	s_waitcnt lgkmcnt(0)
	v_mfma_f32_16x16x32_bf16 v[62:65], v[154:157], v[186:189], v[62:65]
	v_mfma_f32_16x16x32_bf16 v[58:61], v[162:165], v[186:189], v[58:61]
	v_mfma_f32_16x16x32_bf16 v[46:49], v[154:157], v[194:197], v[46:49]
	v_mfma_f32_16x16x32_bf16 v[42:45], v[162:165], v[194:197], v[42:45]
	v_mfma_f32_16x16x32_bf16 v[14:17], v[154:157], v[202:205], v[14:17]
	v_mfma_f32_16x16x32_bf16 v[10:13], v[162:165], v[202:205], v[10:13]
	v_mfma_f32_16x16x32_bf16 v[6:9], v[154:157], v[210:213], v[6:9]
	v_mfma_f32_16x16x32_bf16 v[2:5], v[162:165], v[210:213], v[2:5]
	v_mfma_f32_16x16x32_bf16 v[62:65], v[158:161], v[190:193], v[62:65]
	v_mfma_f32_16x16x32_bf16 v[58:61], v[166:169], v[190:193], v[58:61]
	v_mfma_f32_16x16x32_bf16 v[46:49], v[158:161], v[198:201], v[46:49]
	v_mfma_f32_16x16x32_bf16 v[42:45], v[166:169], v[198:201], v[42:45]
	v_mfma_f32_16x16x32_bf16 v[14:17], v[158:161], v[206:209], v[14:17]
	v_mfma_f32_16x16x32_bf16 v[10:13], v[166:169], v[206:209], v[10:13]
	v_mfma_f32_16x16x32_bf16 v[6:9], v[158:161], v[214:217], v[6:9]
	v_mfma_f32_16x16x32_bf16 v[2:5], v[166:169], v[214:217], v[2:5]
	s_setprio 0
	s_setprio 1
	v_mfma_f32_16x16x32_bf16 v[54:57], v[170:173], v[186:189], v[54:57]
	v_mfma_f32_16x16x32_bf16 v[50:53], v[178:181], v[186:189], v[50:53]
	v_mfma_f32_16x16x32_bf16 v[30:33], v[170:173], v[194:197], v[30:33]
	v_mfma_f32_16x16x32_bf16 v[26:29], v[178:181], v[194:197], v[26:29]
	v_mfma_f32_16x16x32_bf16 v[34:37], v[170:173], v[202:205], v[34:37]
	v_mfma_f32_16x16x32_bf16 v[38:41], v[178:181], v[202:205], v[38:41]
	v_mfma_f32_16x16x32_bf16 v[18:21], v[170:173], v[210:213], v[18:21]
	v_mfma_f32_16x16x32_bf16 v[22:25], v[178:181], v[210:213], v[22:25]
	v_mfma_f32_16x16x32_bf16 v[54:57], v[174:177], v[190:193], v[54:57]
	v_mfma_f32_16x16x32_bf16 v[50:53], v[182:185], v[190:193], v[50:53]
	v_mfma_f32_16x16x32_bf16 v[30:33], v[174:177], v[198:201], v[30:33]
	v_mfma_f32_16x16x32_bf16 v[26:29], v[182:185], v[198:201], v[26:29]
	v_mfma_f32_16x16x32_bf16 v[34:37], v[174:177], v[206:209], v[34:37]
	v_mfma_f32_16x16x32_bf16 v[38:41], v[182:185], v[206:209], v[38:41]
	v_mfma_f32_16x16x32_bf16 v[18:21], v[174:177], v[214:217], v[18:21]
	v_mfma_f32_16x16x32_bf16 v[22:25], v[182:185], v[214:217], v[22:25]
.Lms_4:
	s_setprio 0
	s_barrier
	s_cmp_lt_i32 s23, 2
	s_mov_b64 s[34:35], -1
	s_cbranch_scc1 .LBB0_988
	s_cmp_eq_u32 s23, 2
	s_mov_b32 s36, s23
	s_cbranch_scc0 .LBB0_986
	s_waitcnt vmcnt(0)
	v_cmp_lt_u32_e32 vcc, 7, v150
	s_cbranch_vccnz .LBB0_985
	global_load_dword v144, v145, s[30:31] sc1
	s_waitcnt vmcnt(0)
	v_cmp_lt_u32_e32 vcc, 7, v144
	s_cbranch_vccnz .LBB0_985

;     __device__ __forceinline__ bool get(int i, int& pm, int& pn) const { return map((long)i * G + c, pm, pn); }
;     __device__ __forceinline__ bool next(int i, Unit& o) const { if (i != 0) return false; o = u; return true; }
;     __device__ __forceinline__ bool map(long L, int& pm, int& pn) const {
;         if (L >= nwg) return false;
;         const int nig = WGM * nN;
;         int wgid = (int)L; { const int q = nwg / NXCD, r = nwg % NXCD, xcd = wgid % NXCD; int off = wgid / NXCD; const int cs = (xcd < r ? xcd * (q + 1) : r * (q + 1) + (xcd - r) * q), len = q + (xcd < r ? 1 : 0);
;             if (rot) { const int lead = (nig - cs % nig) % nig; if (lead < len) { off += lead; if (off >= len) off -= len; } }
;             wgid = cs + off; }
;         const int gid = wgid / nig, fm = gid * WGM, gsz = (nM - fm) < WGM ? (nM - fm) : WGM;
;         pm = fm + ((wgid % nig) % gsz); pn = (wgid % nig) / gsz; return true;
;     __device__ __forceinline__ bool next(int i, Unit& u) const { int pm, pn;
;         if (GATHER) { if (!o.get(i, pm, pn)) return false; }
;         else { const bool light = o.c >= rem; const long L = (light && i < 2) ? (long)i * nl + (o.c - rem) : 2L * nl + (long)(light ? i - 2 : i) * o.G + o.c; if (!o.map(L, pm, pn)) return false; }
;         const int e = __builtin_amdgcn_readfirstlane(texp[pm]);
;         u.pm = pm; u.pn = pn; u.aux = e; u.kt = KT; u.ui = i; u.rb = (pm - __builtin_amdgcn_readfirstlane(tbase[e])) * 256; u.cn = __builtin_amdgcn_readfirstlane(tcnt[e]);
;         u.A = GATHER ? A : A + (size_t)((unsigned)pm * AT); u.B = B + (size_t)((unsigned)e * BE + (unsigned)pn * BT); return true; }
.LBB0_1484:
	s_or_b64 exec, exec, s[4:5]
	s_add_u32 s10, s6, 0x4a400000
	s_addc_u32 s11, s7, 0
	s_add_u32 s60, s6, 0x11800000
	v_mov_b32_e32 v10, v0
	v_cndmask_b32_e64 v1, 0, 1, s[12:13]
	s_addc_u32 s61, s7, 0
	s_waitcnt lgkmcnt(0)
	s_barrier
	v_cmp_ne_u32_e64 s[2:3], 1, v1
	s_andn2_b64 vcc, exec, s[12:13]
	v_readfirstlane_b32 s4, v10
	s_cbranch_vccnz .LBB0_1486
	s_lshr_b32 s5, s56, 29
	s_add_i32 s5, s51, s5
	s_ashr_i32 s12, s5, 3
	s_and_b32 s5, s5, -8
	s_sub_i32 s5, s51, s5
	s_cmp_lt_i32 s5, 0
	s_cselect_b32 s13, s48, s33
	s_mul_i32 s5, s13, s5
	s_add_i32 s5, s5, s12
	s_ashr_i32 s12, s5, 31
	s_lshr_b32 s12, s12, 26
	s_add_i32 s12, s5, s12
	s_ashr_i32 s13, s12, 6
	s_lshl_b32 s13, s13, 3
	s_sub_i32 s14, s33, s13
	s_min_i32 s14, s14, 8
	s_abs_i32 s15, s14
	v_cvt_f32_u32_e32 v1, s15
	s_sub_i32 s17, 0, s15
	s_andn2_b32 s12, s12, 63
	s_sub_i32 s5, s5, s12
	v_rcp_iflag_f32_e32 v1, v1
	s_abs_i32 s12, s5
	s_xor_b32 s16, s5, s14
	s_ashr_i32 s16, s16, 31
	v_mul_f32_e32 v1, 0x4f7ffffe, v1
	v_cvt_u32_f32_e32 v1, v1
	s_mov_b64 s[34:35], s[10:11]
	v_readfirstlane_b32 s18, v1
	s_mul_i32 s17, s17, s18
	s_mul_hi_u32 s17, s18, s17
	s_add_i32 s18, s18, s17
	s_mul_hi_u32 s17, s12, s18
	s_mul_i32 s18, s17, s15
	s_sub_i32 s12, s12, s18
	s_add_i32 s19, s17, 1
	s_sub_i32 s18, s12, s15
	s_cmp_ge_u32 s12, s15
	s_cselect_b32 s17, s19, s17
	s_cselect_b32 s12, s18, s12
	s_add_i32 s18, s17, 1
	s_cmp_ge_u32 s12, s15
	s_cselect_b32 s12, s18, s17
	s_xor_b32 s12, s12, s16
	s_sub_i32 s77, s12, s16
	s_mul_i32 s12, s77, s14
	s_sub_i32 s5, s5, s12
	s_add_i32 s62, s5, s13
	s_lshl_b32 s5, s62, 2
	s_add_i32 s5, s5, 0
	s_add_i32 s5, s5, 0x20240
	v_mov_b32_e32 v1, s5
	ds_read_b32 v1, v1
	s_lshl_b32 s5, s77, 20
	s_waitcnt lgkmcnt(0)
	v_readfirstlane_b32 s12, v1
	s_lshl_b32 s98, s12, 2
	v_mov_b32_e32 v251, s98
	v_add_u32_e32 v251, 0x20100, v251
	ds_read_b32 v252, v251
	ds_read_b32 v253, v251 offset:128
	s_waitcnt lgkmcnt(0)
	v_readfirstlane_b32 s98, v252
	v_readfirstlane_b32 s100, v253
	s_nop 3
	s_sub_i32 s100, s62, s100
	s_lshl_b32 s100, s100, 8
	s_sub_i32 s98, s98, s100
	s_cmp_le_i32 s98, 128
	s_cselect_b32 s98, 1, 0
	s_lshl_b32 s12, s12, 23
	s_add_i32 s12, s12, s5
	s_add_u32 s40, s60, s12
	s_addc_u32 s41, s61, 0
	s_and_b64 vcc, exec, s[2:3]
	s_cbranch_vccz .LBB0_1487
	s_branch .LBB0_1537

;     __device__ __forceinline__ bool get(int i, int& pm, int& pn) const { return map((long)i * G + c, pm, pn); }
;     __device__ __forceinline__ bool next(int i, Unit& o) const { if (i != 0) return false; o = u; return true; }
;     __device__ __forceinline__ bool map(long L, int& pm, int& pn) const {
;         if (L >= nwg) return false;
;         const int nig = WGM * nN;
;         int wgid = (int)L; { const int q = nwg / NXCD, r = nwg % NXCD, xcd = wgid % NXCD; int off = wgid / NXCD; const int cs = (xcd < r ? xcd * (q + 1) : r * (q + 1) + (xcd - r) * q), len = q + (xcd < r ? 1 : 0);
;             if (rot) { const int lead = (nig - cs % nig) % nig; if (lead < len) { off += lead; if (off >= len) off -= len; } }
;             wgid = cs + off; }
;         const int gid = wgid / nig, fm = gid * WGM, gsz = (nM - fm) < WGM ? (nM - fm) : WGM;
;         pm = fm + ((wgid % nig) % gsz); pn = (wgid % nig) / gsz; return true;
;     __device__ __forceinline__ bool next(int i, Unit& u) const { int pm, pn;
;         if (GATHER) { if (!o.get(i, pm, pn)) return false; }
;         else { const bool light = o.c >= rem; const long L = (light && i < 2) ? (long)i * nl + (o.c - rem) : 2L * nl + (long)(light ? i - 2 : i) * o.G + o.c; if (!o.map(L, pm, pn)) return false; }
;         const int e = __builtin_amdgcn_readfirstlane(texp[pm]);
;         u.pm = pm; u.pn = pn; u.aux = e; u.kt = KT; u.ui = i; u.rb = (pm - __builtin_amdgcn_readfirstlane(tbase[e])) * 256; u.cn = __builtin_amdgcn_readfirstlane(tcnt[e]);
;         u.A = GATHER ? A : A + (size_t)((unsigned)pm * AT); u.B = B + (size_t)((unsigned)e * BE + (unsigned)pn * BT); return true; }
.LBB0_1595:
	s_or_b64 exec, exec, s[6:7]
	s_add_u32 s11, s14, 0x59000000
	s_addc_u32 s38, s15, 0
	s_add_u32 s39, s14, 0x29800000
	s_waitcnt vmcnt(0)
	v_mov_b32_e32 v1, v0
	v_cndmask_b32_e64 v2, 0, 1, s[2:3]
	s_addc_u32 s40, s15, 0
	s_waitcnt lgkmcnt(0)
	s_barrier
	v_cmp_ne_u32_e64 s[4:5], 1, v2
	s_andn2_b64 vcc, exec, s[2:3]
	v_readfirstlane_b32 s18, v1
	s_cbranch_vccnz .LBB0_1597
	s_ashr_i32 s2, s16, 31
	s_lshr_b32 s2, s2, 29
	s_add_i32 s2, s16, s2
	s_ashr_i32 s3, s2, 3
	s_and_b32 s2, s2, -8
	s_sub_i32 s2, s16, s2
	s_cmp_lt_i32 s2, 0
	s_cselect_b32 s6, s48, s33
	s_mul_i32 s6, s6, s2
	s_ashr_i32 s7, s6, 31
	s_lshr_b32 s7, s7, 26
	s_add_i32 s7, s6, s7
	s_andn2_b32 s7, s7, 63
	s_lshr_b32 s2, s2, 31
	s_sub_i32 s7, s6, s7
	s_add_i32 s2, s2, s33
	s_sub_i32 s16, 64, s7
	s_sub_i32 s7, 0, s7
	s_cmp_lt_u32 s16, 64
	s_cselect_b32 s7, s16, s7
	s_add_i32 s16, s7, s3
	s_cmp_ge_i32 s16, s2
	s_cselect_b32 s17, s2, 0
	s_sub_i32 s16, s16, s17
	s_cmp_lt_i32 s7, s2
	s_cselect_b32 s2, s16, s3
	s_add_i32 s2, s2, s6
	s_ashr_i32 s3, s2, 31
	s_lshr_b32 s3, s3, 26
	s_add_i32 s3, s2, s3
	s_ashr_i32 s6, s3, 6
	s_lshl_b32 s6, s6, 3
	s_sub_i32 s7, s33, s6
	s_min_i32 s7, s7, 8
	s_abs_i32 s16, s7
	v_cvt_f32_u32_e32 v2, s16
	s_sub_i32 s19, 0, s16
	s_andn2_b32 s3, s3, 63
	s_sub_i32 s2, s2, s3
	v_rcp_iflag_f32_e32 v2, v2
	s_abs_i32 s17, s2
	s_xor_b32 s3, s2, s7
	s_ashr_i32 s3, s3, 31
	v_mul_f32_e32 v2, 0x4f7ffffe, v2
	v_cvt_u32_f32_e32 v2, v2
	s_nop 0
	v_readfirstlane_b32 s20, v2
	s_mul_i32 s19, s19, s20
	s_mul_hi_u32 s19, s20, s19
	s_add_i32 s20, s20, s19
	s_mul_hi_u32 s19, s17, s20
	s_mul_i32 s20, s19, s16
	s_sub_i32 s17, s17, s20
	s_add_i32 s20, s19, 1
	s_sub_i32 s21, s17, s16
	s_cmp_ge_u32 s17, s16
	s_cselect_b32 s19, s20, s19
	s_cselect_b32 s17, s21, s17
	s_add_i32 s20, s19, 1
	s_cmp_ge_u32 s17, s16
	s_cselect_b32 s16, s20, s19
	s_xor_b32 s16, s16, s3
	s_sub_i32 s64, s16, s3
	s_mul_i32 s3, s64, s7
	s_sub_i32 s2, s2, s3
	s_add_i32 s2, s2, s6
	s_lshl_b32 s3, s2, 2
	s_add_i32 s3, s3, 0
	s_add_i32 s3, s3, 0x20240
	v_mov_b32_e32 v2, s3
	ds_read_b32 v2, v2
	s_lshl_b32 s3, s2, 19
	s_add_u32 s26, s11, s3
	s_addc_u32 s27, s38, 0
	s_waitcnt lgkmcnt(0)
	v_readfirstlane_b32 s6, v2
	s_lshl_b32 s98, s6, 2
	v_mov_b32_e32 v251, s98
	v_add_u32_e32 v251, 0x20100, v251
	ds_read_b32 v252, v251
	ds_read_b32 v253, v251 offset:128
	s_waitcnt lgkmcnt(0)
	v_readfirstlane_b32 s98, v252
	v_readfirstlane_b32 s100, v253
	s_nop 3
	s_sub_i32 s100, s2, s100
	s_lshl_b32 s100, s100, 8
	s_sub_i32 s98, s98, s100
	s_cmp_le_i32 s98, 128
	s_cselect_b32 s98, 1, 0
	s_lshl_b32 s3, s6, 22
	s_lshl_b32 s6, s64, 19
	s_add_i32 s3, s3, s6
	s_add_u32 s28, s39, s3
	s_addc_u32 s29, s40, 0
	s_lshl_b32 s2, s2, 5
	s_ashr_i32 s3, s2, 31
	s_and_b64 vcc, exec, s[4:5]
	s_cbranch_vccz .LBB0_1598
	s_branch .LBB0_1647
